# P8 fused epilogue residual loads prefetched two row groups ahead; P15 gather issues its 16 row-chunk loads up front
# speedup vs baseline: 1.0091x; 1.0012x over previous
.LBB0_934:
	v_readlane_b32 s68, v251, 11
	v_readlane_b32 s70, v251, 13
	v_readlane_b32 s71, v251, 14
	s_mov_b64 s[2:3], s[70:71]
	v_readlane_b32 s69, v251, 12
	s_add_u32 s18, s2, 0x2000
	s_addc_u32 s19, s3, 0
	v_lshrrev_b32_e32 v2, 1, v0
	s_lshl_b32 s0, s64, 5
	s_lshl_b32 s61, s26, 8
	s_lshl_b32 s69, s35, 8
	v_and_b32_e32 v175, 24, v2
	s_or_b32 s0, s0, s61
	v_add_u32_e32 v164, s69, v177
	v_mov_b32_e32 v165, 0
	v_or_b32_e32 v162, s0, v175
	v_lshlrev_b64 v[2:3], 12, v[164:165]
	v_ashrrev_i32_e32 v163, 31, v162
	v_lshl_add_u64 v[2:3], s[22:23], 0, v[2:3]
	s_nop 15
	s_nop 7
	v_lshl_add_u64 v[166:167], v[162:163], 1, v[2:3]
	s_waitcnt vmcnt(0)
	s_barrier
	global_load_dwordx4 v[18:21], v[166:167], off
	v_mov_b32_e32 v248, v166
	v_mov_b32_e32 v249, v167
	global_load_dwordx4 v[22:25], v[166:167], off offset:256
	v_lshl_add_u64 v[2:3], v[162:163], 2, s[18:19]
	global_load_dwordx4 v[14:17], v[2:3], off
	global_load_dwordx4 v[10:13], v[2:3], off offset:16
	global_load_dwordx4 v[6:9], v[2:3], off offset:512
	s_nop 0
	global_load_dwordx4 v[2:5], v[2:3], off offset:528
	s_mov_b32 s98, 0x10000
	s_mov_b32 s99, 0
	v_lshl_add_u64 v[230:231], v[248:249], 0, s[98:99]
	global_load_dwordx4 v[226:229], v[230:231], off
	global_load_dwordx4 v[230:233], v[230:231], off offset:256
	s_mov_b32 s98, 0x20000
	s_mov_b32 s99, 0
	v_lshl_add_u64 v[238:239], v[248:249], 0, s[98:99]
	global_load_dwordx4 v[234:237], v[238:239], off
	global_load_dwordx4 v[238:241], v[238:239], off offset:256
	v_mbcnt_lo_u32_b32 v26, -1, 0
	v_mbcnt_hi_u32_b32 v26, -1, v26
	v_and_b32_e32 v28, 64, v26
	v_xor_b32_e32 v27, 16, v26
	v_add_u32_e32 v28, 64, v28
	v_xor_b32_e32 v29, 32, v26
	v_cmp_lt_i32_e32 vcc, v27, v28
	s_brev_b32 s0, 60
	s_lshl_b32 s1, s64, 3
	v_cndmask_b32_e32 v27, v26, v27, vcc
	v_cmp_lt_i32_e32 vcc, v29, v28
	v_lshlrev_b32_e32 v169, 2, v27
	v_cmp_gt_u32_e64 s[2:3], 16, v1
	v_cndmask_b32_e32 v26, v26, v29, vcc
	v_lshlrev_b32_e32 v168, 2, v26
	s_add_i32 s6, s1, 0
	v_readlane_b32 s72, v251, 15
	v_readlane_b32 s73, v251, 16
	v_readlane_b32 s74, v251, 17
	v_readlane_b32 s75, v251, 18
	v_readlane_b32 s76, v251, 19
	v_readlane_b32 s77, v251, 20
	v_readlane_b32 s78, v251, 21
	v_readlane_b32 s79, v251, 22
	v_readlane_b32 s80, v251, 23
	v_readlane_b32 s81, v251, 24
	v_readlane_b32 s82, v251, 25
	v_readlane_b32 s83, v251, 26
	s_waitcnt vmcnt(4)
	v_lshlrev_b32_e32 v26, 16, v18
	v_and_b32_e32 v27, 0xffff0000, v18
	v_lshlrev_b32_e32 v18, 16, v19
	v_and_b32_e32 v19, 0xffff0000, v19
	v_lshlrev_b32_e32 v178, 16, v20
	v_and_b32_e32 v179, 0xffff0000, v20
	v_lshlrev_b32_e32 v20, 16, v21
	v_and_b32_e32 v21, 0xffff0000, v21
	v_lshlrev_b32_e32 v180, 16, v22
	v_and_b32_e32 v181, 0xffff0000, v22
	v_lshlrev_b32_e32 v22, 16, v23
	v_and_b32_e32 v23, 0xffff0000, v23
	v_pk_fma_f32 v[32:33], v[152:153], s[0:1], v[18:19] op_sel_hi:[1,0,1]
	v_pk_fma_f32 v[30:31], v[150:151], s[0:1], v[26:27] op_sel_hi:[1,0,1]
	v_pk_fma_f32 v[28:29], v[156:157], s[0:1], v[20:21] op_sel_hi:[1,0,1]
	v_pk_fma_f32 v[26:27], v[154:155], s[0:1], v[178:179] op_sel_hi:[1,0,1]
	v_pk_fma_f32 v[20:21], v[160:161], s[0:1], v[22:23] op_sel_hi:[1,0,1]
	v_pk_fma_f32 v[18:19], v[158:159], s[0:1], v[180:181] op_sel_hi:[1,0,1]
	v_mul_f32_e32 v176, v31, v31
	v_mul_f32_e32 v180, v33, v33
	v_pk_mul_f32 v[22:23], v[16:17], v[32:33]
	v_mul_f32_e32 v181, v27, v27
	v_mul_f32_e32 v182, v29, v29
	v_pk_mul_f32 v[156:157], v[12:13], v[28:29]
	v_pk_mul_f32 v[154:155], v[14:15], v[30:31]
	v_pk_mul_f32 v[158:159], v[10:11], v[26:27]
	v_fmac_f32_e32 v176, v30, v30
	v_fmac_f32_e32 v180, v32, v32
	v_max_f32_e64 v22, |v22|, |v23|
	v_fmac_f32_e32 v181, v26, v26
	v_fmac_f32_e32 v182, v28, v28
	v_max_f32_e64 v23, |v156|, |v157|
	v_add_f32_e32 v157, v176, v180
	v_max3_f32 v22, |v154|, |v155|, v22
	v_add_f32_e32 v154, v181, v182
	v_max3_f32 v23, |v158|, |v159|, v23
	v_add_f32_e32 v154, v157, v154
	v_max3_f32 v157, v22, 0, v23
	v_lshlrev_b32_e32 v22, 16, v24
	v_and_b32_e32 v23, 0xffff0000, v24
	v_lshlrev_b32_e32 v24, 16, v25
	v_and_b32_e32 v25, 0xffff0000, v25
	v_mul_f32_e32 v183, v19, v19
	v_mul_f32_e32 v184, v21, v21
	v_pk_fma_f32 v[24:25], v[148:149], s[0:1], v[24:25] op_sel_hi:[1,0,1]
	v_pk_fma_f32 v[22:23], v[146:147], s[0:1], v[22:23] op_sel_hi:[1,0,1]
	v_fmac_f32_e32 v183, v18, v18
	v_fmac_f32_e32 v184, v20, v20
	v_mul_f32_e32 v146, v23, v23
	v_mul_f32_e32 v147, v25, v25
	v_add_f32_e32 v155, v183, v184
	v_fmac_f32_e32 v146, v22, v22
	v_fmac_f32_e32 v147, v24, v24
	v_add_f32_e32 v154, v154, v155
	v_add_f32_e32 v146, v146, v147
	v_pk_mul_f32 v[160:161], v[8:9], v[20:21]
	v_add_f32_e32 v154, v154, v146
	v_pk_mul_f32 v[146:147], v[4:5], v[24:25]
	v_pk_mul_f32 v[178:179], v[6:7], v[18:19]
	v_max_f32_e64 v156, |v160|, |v161|
	v_pk_mul_f32 v[148:149], v[2:3], v[22:23]
	v_max_f32_e64 v146, |v146|, |v147|
	v_max3_f32 v156, |v178|, |v179|, v156
	v_max3_f32 v146, |v148|, |v149|, v146
	v_max3_f32 v148, v157, v156, v146
	ds_bpermute_b32 v149, v169, v148
	ds_bpermute_b32 v147, v169, v154
	v_cvt_pk_bf16_f32 v150, v30, v31
	v_cvt_pk_bf16_f32 v151, v32, v33
	v_cvt_pk_bf16_f32 v152, v26, v27
	s_waitcnt lgkmcnt(1)
	v_max_f32_e32 v149, v149, v149
	s_waitcnt lgkmcnt(0)
	v_add_f32_e32 v146, v154, v147
	v_max_f32_e32 v148, v148, v149
	ds_bpermute_b32 v147, v168, v146
	ds_bpermute_b32 v149, v168, v148
	v_cvt_pk_bf16_f32 v153, v28, v29
	global_store_dwordx4 v[166:167], v[150:153], off
	s_nop 1
	v_cvt_pk_bf16_f32 v150, v18, v19
	v_cvt_pk_bf16_f32 v151, v20, v21
	v_cvt_pk_bf16_f32 v152, v22, v23
	v_cvt_pk_bf16_f32 v153, v24, v25
	global_store_dwordx4 v[166:167], v[150:153], off offset:256
	s_and_saveexec_b64 s[4:5], s[2:3]
	s_cbranch_execz .LBB0_936
	s_waitcnt lgkmcnt(1)
	v_add_f32_e32 v146, v146, v147
	s_waitcnt lgkmcnt(0)
	v_max_f32_e32 v147, v149, v149
	v_max_f32_e32 v148, v148, v148
	v_lshl_add_u32 v150, v177, 5, s6
	v_max_f32_e32 v147, v148, v147
	ds_write_b64 v150, v[146:147]
.LBB0_936:
	s_or_b64 exec, exec, s[4:5]
	v_or_b32_e32 v148, 16, v177
	v_add_u32_e32 v146, s69, v148
	s_waitcnt lgkmcnt(1)
	v_mov_b32_e32 v147, v165
	v_lshlrev_b64 v[150:151], 12, v[146:147]
	v_lshl_add_u64 v[150:151], s[22:23], 0, v[150:151]
	v_lshl_add_u64 v[158:159], v[162:163], 1, v[150:151]
	s_mov_b32 s98, 0x30000
	s_mov_b32 s99, 0
	v_lshl_add_u64 v[222:223], v[248:249], 0, s[98:99]
	global_load_dwordx4 v[218:221], v[222:223], off
	global_load_dwordx4 v[222:225], v[222:223], off offset:256
	s_waitcnt vmcnt(7)
	v_mov_b32_e32 v150, v226
	v_mov_b32_e32 v151, v227
	v_mov_b32_e32 v152, v228
	v_mov_b32_e32 v153, v229
	v_lshlrev_b32_e32 v160, 16, v150
	v_and_b32_e32 v161, 0xffff0000, v150
	v_lshlrev_b32_e32 v150, 16, v151
	v_and_b32_e32 v151, 0xffff0000, v151
	v_lshlrev_b32_e32 v166, 16, v152
	v_and_b32_e32 v167, 0xffff0000, v152
	v_lshlrev_b32_e32 v152, 16, v153
	v_and_b32_e32 v153, 0xffff0000, v153
	s_waitcnt vmcnt(6)
	v_mov_b32_e32 v154, v230
	v_mov_b32_e32 v155, v231
	v_mov_b32_e32 v156, v232
	v_mov_b32_e32 v157, v233
	v_lshlrev_b32_e32 v178, 16, v154
	v_and_b32_e32 v179, 0xffff0000, v154
	v_lshlrev_b32_e32 v154, 16, v155
	v_and_b32_e32 v155, 0xffff0000, v155
	v_lshlrev_b32_e32 v180, 16, v156
	v_and_b32_e32 v181, 0xffff0000, v156
	v_lshlrev_b32_e32 v156, 16, v157
	v_and_b32_e32 v157, 0xffff0000, v157
	v_pk_fma_f32 v[128:129], v[128:129], s[0:1], v[150:151] op_sel_hi:[1,0,1]
	v_pk_fma_f32 v[126:127], v[126:127], s[0:1], v[160:161] op_sel_hi:[1,0,1]
	v_pk_fma_f32 v[124:125], v[124:125], s[0:1], v[152:153] op_sel_hi:[1,0,1]
	v_pk_fma_f32 v[122:123], v[122:123], s[0:1], v[166:167] op_sel_hi:[1,0,1]
	v_pk_fma_f32 v[104:105], v[104:105], s[0:1], v[154:155] op_sel_hi:[1,0,1]
	v_pk_fma_f32 v[102:103], v[102:103], s[0:1], v[178:179] op_sel_hi:[1,0,1]
	v_pk_fma_f32 v[100:101], v[100:101], s[0:1], v[156:157] op_sel_hi:[1,0,1]
	s_waitcnt lgkmcnt(0)
	v_mul_f32_e32 v149, v127, v127
	v_mul_f32_e32 v153, v129, v129
	v_pk_mul_f32 v[154:155], v[16:17], v[128:129]
	v_mul_f32_e32 v176, v123, v123
	v_mul_f32_e32 v186, v125, v125
	v_pk_mul_f32 v[160:161], v[12:13], v[124:125]
	v_pk_fma_f32 v[98:99], v[98:99], s[0:1], v[180:181] op_sel_hi:[1,0,1]
	v_pk_mul_f32 v[156:157], v[14:15], v[126:127]
	v_pk_mul_f32 v[166:167], v[10:11], v[122:123]
	v_mul_f32_e32 v187, v103, v103
	v_mul_f32_e32 v188, v105, v105
	v_pk_mul_f32 v[178:179], v[8:9], v[104:105]
	v_pk_mul_f32 v[182:183], v[4:5], v[100:101]
	v_fmac_f32_e32 v149, v126, v126
	v_fmac_f32_e32 v153, v128, v128
	v_max_f32_e64 v154, |v154|, |v155|
	v_fmac_f32_e32 v176, v122, v122
	v_fmac_f32_e32 v186, v124, v124
	v_max_f32_e64 v155, |v160|, |v161|
	v_pk_mul_f32 v[180:181], v[6:7], v[102:103]
	v_mul_f32_e32 v189, v99, v99
	v_mul_f32_e32 v190, v101, v101
	v_pk_mul_f32 v[184:185], v[2:3], v[98:99]
	v_fmac_f32_e32 v187, v102, v102
	v_fmac_f32_e32 v188, v104, v104
	v_max_f32_e64 v160, |v178|, |v179|
	v_max_f32_e64 v161, |v182|, |v183|
	v_add_f32_e32 v149, v149, v153
	v_max3_f32 v153, |v156|, |v157|, v154
	v_add_f32_e32 v154, v176, v186
	v_max3_f32 v155, |v166|, |v167|, v155
	v_fmac_f32_e32 v189, v98, v98
	v_fmac_f32_e32 v190, v100, v100
	v_add_f32_e32 v156, v187, v188
	v_max3_f32 v157, |v180|, |v181|, v160
	v_max3_f32 v161, |v184|, |v185|, v161
	v_add_f32_e32 v149, v149, v154
	v_max3_f32 v153, v153, 0, v155
	v_add_f32_e32 v160, v189, v190
	v_add_f32_e32 v149, v149, v156
	v_max3_f32 v155, v153, v157, v161
	v_add_f32_e32 v149, v149, v160
	ds_bpermute_b32 v156, v169, v155
	ds_bpermute_b32 v157, v169, v149
	v_cvt_pk_bf16_f32 v150, v126, v127
	v_cvt_pk_bf16_f32 v151, v128, v129
	v_cvt_pk_bf16_f32 v152, v122, v123
	v_cvt_pk_bf16_f32 v153, v124, v125
	global_store_dwordx4 v[158:159], v[150:153], off
	v_cvt_pk_bf16_f32 v154, v102, v103
	s_waitcnt lgkmcnt(1)
	v_max_f32_e32 v151, v156, v156
	s_waitcnt lgkmcnt(0)
	v_add_f32_e32 v150, v149, v157
	v_max_f32_e32 v149, v155, v151
	ds_bpermute_b32 v151, v168, v150
	ds_bpermute_b32 v152, v168, v149
	v_cvt_pk_bf16_f32 v155, v104, v105
	v_cvt_pk_bf16_f32 v156, v98, v99
	v_cvt_pk_bf16_f32 v157, v100, v101
	global_store_dwordx4 v[158:159], v[154:157], off offset:256
	s_and_saveexec_b64 s[0:1], s[2:3]
	s_cbranch_execz .LBB0_938
	v_lshl_add_u32 v153, v148, 5, s6
	s_waitcnt lgkmcnt(1)
	v_add_f32_e32 v148, v150, v151
	s_waitcnt lgkmcnt(0)
	v_max_f32_e32 v150, v152, v152
	v_max_f32_e32 v149, v149, v149
	v_max_f32_e32 v149, v149, v150
	ds_write_b64 v153, v[148:149]
.LBB0_938:
	s_or_b64 exec, exec, s[0:1]
	v_or_b32_e32 v150, 32, v177
	v_add_u32_e32 v148, s69, v150
	v_mov_b32_e32 v149, 0
	s_waitcnt lgkmcnt(0)
	v_lshlrev_b64 v[152:153], 12, v[148:149]
	v_lshl_add_u64 v[152:153], s[22:23], 0, v[152:153]
	v_lshl_add_u64 v[160:161], v[162:163], 1, v[152:153]
	s_mov_b32 s98, 0x80000
	s_mov_b32 s99, 0
	v_lshl_add_u64 v[230:231], v[248:249], 0, s[98:99]
	global_load_dwordx4 v[226:229], v[230:231], off
	global_load_dwordx4 v[230:233], v[230:231], off offset:256
	s_brev_b32 s0, 60
	s_waitcnt vmcnt(9)
	v_mov_b32_e32 v152, v234
	v_mov_b32_e32 v153, v235
	v_mov_b32_e32 v154, v236
	v_mov_b32_e32 v155, v237
	v_lshlrev_b32_e32 v166, 16, v152
	v_and_b32_e32 v167, 0xffff0000, v152
	v_lshlrev_b32_e32 v152, 16, v153
	v_and_b32_e32 v153, 0xffff0000, v153
	v_lshlrev_b32_e32 v178, 16, v154
	v_and_b32_e32 v179, 0xffff0000, v154
	v_lshlrev_b32_e32 v154, 16, v155
	v_and_b32_e32 v155, 0xffff0000, v155
	s_waitcnt vmcnt(8)
	v_mov_b32_e32 v156, v238
	v_mov_b32_e32 v157, v239
	v_mov_b32_e32 v158, v240
	v_mov_b32_e32 v159, v241
	v_lshlrev_b32_e32 v180, 16, v156
	v_and_b32_e32 v181, 0xffff0000, v156
	v_lshlrev_b32_e32 v156, 16, v157
	v_and_b32_e32 v157, 0xffff0000, v157
	v_lshlrev_b32_e32 v182, 16, v158
	v_and_b32_e32 v183, 0xffff0000, v158
	v_lshlrev_b32_e32 v158, 16, v159
	v_and_b32_e32 v159, 0xffff0000, v159
	v_pk_fma_f32 v[144:145], v[144:145], s[0:1], v[152:153] op_sel_hi:[1,0,1]
	v_pk_fma_f32 v[142:143], v[142:143], s[0:1], v[166:167] op_sel_hi:[1,0,1]
	v_pk_fma_f32 v[140:141], v[140:141], s[0:1], v[154:155] op_sel_hi:[1,0,1]
	v_pk_fma_f32 v[138:139], v[138:139], s[0:1], v[178:179] op_sel_hi:[1,0,1]
	v_pk_fma_f32 v[136:137], v[136:137], s[0:1], v[156:157] op_sel_hi:[1,0,1]
	v_pk_fma_f32 v[134:135], v[134:135], s[0:1], v[180:181] op_sel_hi:[1,0,1]
	v_pk_fma_f32 v[132:133], v[132:133], s[0:1], v[158:159] op_sel_hi:[1,0,1]
	v_mul_f32_e32 v151, v143, v143
	v_mul_f32_e32 v155, v145, v145
	v_pk_mul_f32 v[156:157], v[16:17], v[144:145]
	v_mul_f32_e32 v176, v139, v139
	v_mul_f32_e32 v188, v141, v141
	v_pk_mul_f32 v[166:167], v[12:13], v[140:141]
	v_pk_fma_f32 v[130:131], v[130:131], s[0:1], v[182:183] op_sel_hi:[1,0,1]
	v_pk_mul_f32 v[158:159], v[14:15], v[142:143]
	v_pk_mul_f32 v[178:179], v[10:11], v[138:139]
	v_mul_f32_e32 v189, v135, v135
	v_mul_f32_e32 v190, v137, v137
	v_pk_mul_f32 v[180:181], v[8:9], v[136:137]
	v_pk_mul_f32 v[184:185], v[4:5], v[132:133]
	v_fmac_f32_e32 v151, v142, v142
	v_fmac_f32_e32 v155, v144, v144
	v_max_f32_e64 v156, |v156|, |v157|
	v_fmac_f32_e32 v176, v138, v138
	v_fmac_f32_e32 v188, v140, v140
	v_max_f32_e64 v157, |v166|, |v167|
	v_pk_mul_f32 v[182:183], v[6:7], v[134:135]
	v_mul_f32_e32 v191, v131, v131
	v_mul_f32_e32 v192, v133, v133
	v_pk_mul_f32 v[186:187], v[2:3], v[130:131]
	v_fmac_f32_e32 v189, v134, v134
	v_fmac_f32_e32 v190, v136, v136
	v_max_f32_e64 v166, |v180|, |v181|
	v_max_f32_e64 v167, |v184|, |v185|
	v_add_f32_e32 v151, v151, v155
	v_max3_f32 v155, |v158|, |v159|, v156
	v_add_f32_e32 v156, v176, v188
	v_max3_f32 v157, |v178|, |v179|, v157
	v_fmac_f32_e32 v191, v130, v130
	v_fmac_f32_e32 v192, v132, v132
	v_add_f32_e32 v158, v189, v190
	v_max3_f32 v159, |v182|, |v183|, v166
	v_max3_f32 v167, |v186|, |v187|, v167
	v_add_f32_e32 v151, v151, v156
	v_max3_f32 v155, v155, 0, v157
	v_add_f32_e32 v166, v191, v192
	v_add_f32_e32 v151, v151, v158
	v_max3_f32 v157, v155, v159, v167
	v_add_f32_e32 v151, v151, v166
	ds_bpermute_b32 v158, v169, v157
	ds_bpermute_b32 v159, v169, v151
	v_cvt_pk_bf16_f32 v152, v142, v143
	v_cvt_pk_bf16_f32 v153, v144, v145
	v_cvt_pk_bf16_f32 v154, v138, v139
	v_cvt_pk_bf16_f32 v155, v140, v141
	global_store_dwordx4 v[160:161], v[152:155], off
	v_cvt_pk_bf16_f32 v156, v134, v135
	s_waitcnt lgkmcnt(1)
	v_max_f32_e32 v153, v158, v158
	s_waitcnt lgkmcnt(0)
	v_add_f32_e32 v152, v151, v159
	v_max_f32_e32 v151, v157, v153
	ds_bpermute_b32 v153, v168, v152
	ds_bpermute_b32 v154, v168, v151
	v_cvt_pk_bf16_f32 v157, v136, v137
	v_cvt_pk_bf16_f32 v158, v130, v131
	v_cvt_pk_bf16_f32 v159, v132, v133
	global_store_dwordx4 v[160:161], v[156:159], off offset:256
	s_and_saveexec_b64 s[4:5], s[2:3]
	s_cbranch_execz .LBB0_940
	v_lshl_add_u32 v155, v150, 5, s6
	s_waitcnt lgkmcnt(1)
	v_add_f32_e32 v150, v152, v153
	s_waitcnt lgkmcnt(0)
	v_max_f32_e32 v152, v154, v154
	v_max_f32_e32 v151, v151, v151
	v_max_f32_e32 v151, v151, v152
	ds_write_b64 v155, v[150:151]
.LBB0_940:
	s_or_b64 exec, exec, s[4:5]
	v_or_b32_e32 v152, 48, v177
	v_add_u32_e32 v150, s69, v152
	v_mov_b32_e32 v151, v149
	s_waitcnt lgkmcnt(0)
	v_lshlrev_b64 v[154:155], 12, v[150:151]
	v_lshl_add_u64 v[154:155], s[22:23], 0, v[154:155]
	v_lshl_add_u64 v[166:167], v[162:163], 1, v[154:155]
	s_mov_b32 s98, 0x90000
	s_mov_b32 s99, 0
	v_lshl_add_u64 v[238:239], v[248:249], 0, s[98:99]
	global_load_dwordx4 v[234:237], v[238:239], off
	global_load_dwordx4 v[238:241], v[238:239], off offset:256
	s_waitcnt vmcnt(9)
	v_mov_b32_e32 v154, v218
	v_mov_b32_e32 v155, v219
	v_mov_b32_e32 v156, v220
	v_mov_b32_e32 v157, v221
	v_lshlrev_b32_e32 v178, 16, v154
	v_and_b32_e32 v179, 0xffff0000, v154
	v_lshlrev_b32_e32 v154, 16, v155
	v_and_b32_e32 v155, 0xffff0000, v155
	v_lshlrev_b32_e32 v180, 16, v156
	v_and_b32_e32 v181, 0xffff0000, v156
	v_lshlrev_b32_e32 v156, 16, v157
	v_and_b32_e32 v157, 0xffff0000, v157
	s_waitcnt vmcnt(8)
	v_mov_b32_e32 v158, v222
	v_mov_b32_e32 v159, v223
	v_mov_b32_e32 v160, v224
	v_mov_b32_e32 v161, v225
	v_lshlrev_b32_e32 v182, 16, v158
	v_and_b32_e32 v183, 0xffff0000, v158
	v_lshlrev_b32_e32 v158, 16, v159
	v_and_b32_e32 v159, 0xffff0000, v159
	v_lshlrev_b32_e32 v184, 16, v160
	v_and_b32_e32 v185, 0xffff0000, v160
	v_lshlrev_b32_e32 v160, 16, v161
	v_and_b32_e32 v161, 0xffff0000, v161
	v_pk_fma_f32 v[120:121], v[120:121], s[0:1], v[154:155] op_sel_hi:[1,0,1]
	v_pk_fma_f32 v[118:119], v[118:119], s[0:1], v[178:179] op_sel_hi:[1,0,1]
	v_pk_fma_f32 v[116:117], v[116:117], s[0:1], v[156:157] op_sel_hi:[1,0,1]
	v_pk_fma_f32 v[114:115], v[114:115], s[0:1], v[180:181] op_sel_hi:[1,0,1]
	v_pk_fma_f32 v[112:113], v[112:113], s[0:1], v[158:159] op_sel_hi:[1,0,1]
	v_pk_fma_f32 v[110:111], v[110:111], s[0:1], v[182:183] op_sel_hi:[1,0,1]
	v_pk_fma_f32 v[108:109], v[108:109], s[0:1], v[160:161] op_sel_hi:[1,0,1]
	v_mul_f32_e32 v153, v119, v119
	v_mul_f32_e32 v157, v121, v121
	v_pk_mul_f32 v[158:159], v[16:17], v[120:121]
	v_mul_f32_e32 v176, v115, v115
	v_mul_f32_e32 v190, v117, v117
	v_pk_mul_f32 v[178:179], v[12:13], v[116:117]
	v_pk_fma_f32 v[106:107], v[106:107], s[0:1], v[184:185] op_sel_hi:[1,0,1]
	v_pk_mul_f32 v[160:161], v[14:15], v[118:119]
	v_pk_mul_f32 v[180:181], v[10:11], v[114:115]
	v_mul_f32_e32 v191, v111, v111
	v_mul_f32_e32 v192, v113, v113
	v_pk_mul_f32 v[182:183], v[8:9], v[112:113]
	v_pk_mul_f32 v[186:187], v[4:5], v[108:109]
	v_fmac_f32_e32 v153, v118, v118
	v_fmac_f32_e32 v157, v120, v120
	v_max_f32_e64 v158, |v158|, |v159|
	v_fmac_f32_e32 v176, v114, v114
	v_fmac_f32_e32 v190, v116, v116
	v_max_f32_e64 v159, |v178|, |v179|
	v_pk_mul_f32 v[184:185], v[6:7], v[110:111]
	v_mul_f32_e32 v193, v107, v107
	v_mul_f32_e32 v194, v109, v109
	v_pk_mul_f32 v[188:189], v[2:3], v[106:107]
	v_fmac_f32_e32 v191, v110, v110
	v_fmac_f32_e32 v192, v112, v112
	v_max_f32_e64 v178, |v182|, |v183|
	v_max_f32_e64 v179, |v186|, |v187|
	v_add_f32_e32 v153, v153, v157
	v_max3_f32 v157, |v160|, |v161|, v158
	v_add_f32_e32 v158, v176, v190
	v_max3_f32 v159, |v180|, |v181|, v159
	v_fmac_f32_e32 v193, v106, v106
	v_fmac_f32_e32 v194, v108, v108
	v_add_f32_e32 v160, v191, v192
	v_max3_f32 v161, |v184|, |v185|, v178
	v_max3_f32 v178, |v188|, |v189|, v179
	v_add_f32_e32 v153, v153, v158
	v_max3_f32 v157, v157, 0, v159
	v_add_f32_e32 v176, v193, v194
	v_add_f32_e32 v153, v153, v160
	v_max3_f32 v159, v157, v161, v178
	v_add_f32_e32 v153, v153, v176
	ds_bpermute_b32 v160, v169, v159
	ds_bpermute_b32 v161, v169, v153
	v_cvt_pk_bf16_f32 v154, v118, v119
	v_cvt_pk_bf16_f32 v155, v120, v121
	v_cvt_pk_bf16_f32 v156, v114, v115
	v_cvt_pk_bf16_f32 v157, v116, v117
	global_store_dwordx4 v[166:167], v[154:157], off
	v_cvt_pk_bf16_f32 v158, v110, v111
	s_waitcnt lgkmcnt(1)
	v_max_f32_e32 v155, v160, v160
	s_waitcnt lgkmcnt(0)
	v_add_f32_e32 v154, v153, v161
	v_max_f32_e32 v153, v159, v155
	ds_bpermute_b32 v155, v168, v154
	ds_bpermute_b32 v156, v168, v153
	v_cvt_pk_bf16_f32 v159, v112, v113
	v_cvt_pk_bf16_f32 v160, v106, v107
	v_cvt_pk_bf16_f32 v161, v108, v109
	global_store_dwordx4 v[166:167], v[158:161], off offset:256
	s_and_saveexec_b64 s[0:1], s[2:3]
	s_cbranch_execz .LBB0_942
	v_lshl_add_u32 v157, v152, 5, s6
	s_waitcnt lgkmcnt(1)
	v_add_f32_e32 v152, v154, v155
	s_waitcnt lgkmcnt(0)
	v_max_f32_e32 v154, v156, v156
	v_max_f32_e32 v153, v153, v153
	v_max_f32_e32 v153, v153, v154
	ds_write_b64 v157, v[152:153]
.LBB0_942:
	s_or_b64 exec, exec, s[0:1]
	v_add_u32_e32 v154, 0x80, v177
	v_add_u32_e32 v152, s69, v154
	v_mov_b32_e32 v153, 0
	s_waitcnt lgkmcnt(0)
	v_lshlrev_b64 v[156:157], 12, v[152:153]
	v_lshl_add_u64 v[156:157], s[22:23], 0, v[156:157]
	v_lshl_add_u64 v[160:161], v[162:163], 1, v[156:157]
	s_mov_b32 s98, 0xa0000
	s_mov_b32 s99, 0
	v_lshl_add_u64 v[222:223], v[248:249], 0, s[98:99]
	global_load_dwordx4 v[218:221], v[222:223], off
	global_load_dwordx4 v[222:225], v[222:223], off offset:256
	s_brev_b32 s0, 60
	s_waitcnt vmcnt(9)
	v_mov_b32_e32 v156, v226
	v_mov_b32_e32 v157, v227
	v_mov_b32_e32 v158, v228
	v_mov_b32_e32 v159, v229
	v_lshlrev_b32_e32 v166, 16, v156
	v_and_b32_e32 v167, 0xffff0000, v156
	v_lshlrev_b32_e32 v156, 16, v157
	v_and_b32_e32 v157, 0xffff0000, v157
	v_lshlrev_b32_e32 v182, 16, v158
	v_and_b32_e32 v183, 0xffff0000, v158
	v_lshlrev_b32_e32 v158, 16, v159
	v_and_b32_e32 v159, 0xffff0000, v159
	s_waitcnt vmcnt(8)
	v_mov_b32_e32 v178, v230
	v_mov_b32_e32 v179, v231
	v_mov_b32_e32 v180, v232
	v_mov_b32_e32 v181, v233
	v_lshlrev_b32_e32 v184, 16, v178
	v_and_b32_e32 v185, 0xffff0000, v178
	v_lshlrev_b32_e32 v178, 16, v179
	v_and_b32_e32 v179, 0xffff0000, v179
	v_lshlrev_b32_e32 v186, 16, v180
	v_and_b32_e32 v187, 0xffff0000, v180
	v_lshlrev_b32_e32 v180, 16, v181
	v_and_b32_e32 v181, 0xffff0000, v181
	v_pk_fma_f32 v[96:97], v[96:97], s[0:1], v[156:157] op_sel_hi:[1,0,1]
	v_pk_fma_f32 v[94:95], v[94:95], s[0:1], v[166:167] op_sel_hi:[1,0,1]
	v_pk_fma_f32 v[92:93], v[92:93], s[0:1], v[158:159] op_sel_hi:[1,0,1]
	v_pk_fma_f32 v[90:91], v[90:91], s[0:1], v[182:183] op_sel_hi:[1,0,1]
	v_pk_fma_f32 v[88:89], v[88:89], s[0:1], v[178:179] op_sel_hi:[1,0,1]
	v_pk_fma_f32 v[86:87], v[86:87], s[0:1], v[184:185] op_sel_hi:[1,0,1]
	v_pk_fma_f32 v[84:85], v[84:85], s[0:1], v[180:181] op_sel_hi:[1,0,1]
	v_mul_f32_e32 v155, v95, v95
	v_mul_f32_e32 v159, v97, v97
	v_pk_mul_f32 v[166:167], v[16:17], v[96:97]
	v_mul_f32_e32 v176, v91, v91
	v_mul_f32_e32 v192, v93, v93
	v_pk_mul_f32 v[180:181], v[12:13], v[92:93]
	v_pk_fma_f32 v[82:83], v[82:83], s[0:1], v[186:187] op_sel_hi:[1,0,1]
	v_pk_mul_f32 v[178:179], v[14:15], v[94:95]
	v_pk_mul_f32 v[182:183], v[10:11], v[90:91]
	v_mul_f32_e32 v193, v87, v87
	v_mul_f32_e32 v194, v89, v89
	v_pk_mul_f32 v[184:185], v[8:9], v[88:89]
	v_pk_mul_f32 v[188:189], v[4:5], v[84:85]
	v_fmac_f32_e32 v155, v94, v94
	v_fmac_f32_e32 v159, v96, v96
	v_max_f32_e64 v166, |v166|, |v167|
	v_fmac_f32_e32 v176, v90, v90
	v_fmac_f32_e32 v192, v92, v92
	v_max_f32_e64 v167, |v180|, |v181|
	v_pk_mul_f32 v[186:187], v[6:7], v[86:87]
	v_mul_f32_e32 v195, v83, v83
	v_mul_f32_e32 v196, v85, v85
	v_pk_mul_f32 v[190:191], v[2:3], v[82:83]
	v_fmac_f32_e32 v193, v86, v86
	v_fmac_f32_e32 v194, v88, v88
	v_max_f32_e64 v180, |v184|, |v185|
	v_max_f32_e64 v181, |v188|, |v189|
	v_add_f32_e32 v155, v155, v159
	v_max3_f32 v159, |v178|, |v179|, v166
	v_add_f32_e32 v166, v176, v192
	v_max3_f32 v167, |v182|, |v183|, v167
	v_fmac_f32_e32 v195, v82, v82
	v_fmac_f32_e32 v196, v84, v84
	v_add_f32_e32 v176, v193, v194
	v_max3_f32 v178, |v186|, |v187|, v180
	v_max3_f32 v180, |v190|, |v191|, v181
	v_add_f32_e32 v155, v155, v166
	v_max3_f32 v159, v159, 0, v167
	v_add_f32_e32 v179, v195, v196
	v_add_f32_e32 v155, v155, v176
	v_max3_f32 v166, v159, v178, v180
	v_add_f32_e32 v155, v155, v179
	ds_bpermute_b32 v167, v169, v166
	ds_bpermute_b32 v176, v169, v155
	v_cvt_pk_bf16_f32 v156, v94, v95
	v_cvt_pk_bf16_f32 v157, v96, v97
	v_cvt_pk_bf16_f32 v158, v90, v91
	v_cvt_pk_bf16_f32 v159, v92, v93
	global_store_dwordx4 v[160:161], v[156:159], off
	v_cvt_pk_bf16_f32 v178, v86, v87
	v_cvt_pk_bf16_f32 v179, v88, v89
	s_waitcnt lgkmcnt(1)
	v_max_f32_e32 v157, v167, v167
	s_waitcnt lgkmcnt(0)
	v_add_f32_e32 v156, v155, v176
	v_max_f32_e32 v155, v166, v157
	ds_bpermute_b32 v157, v168, v156
	ds_bpermute_b32 v158, v168, v155
	v_cvt_pk_bf16_f32 v180, v82, v83
	v_cvt_pk_bf16_f32 v181, v84, v85
	global_store_dwordx4 v[160:161], v[178:181], off offset:256
	s_and_saveexec_b64 s[4:5], s[2:3]
	s_cbranch_execz .LBB0_944
	v_lshl_add_u32 v159, v154, 5, s6
	s_waitcnt lgkmcnt(1)
	v_add_f32_e32 v154, v156, v157
	s_waitcnt lgkmcnt(0)
	v_max_f32_e32 v156, v158, v158
	v_max_f32_e32 v155, v155, v155
	v_max_f32_e32 v155, v155, v156
	ds_write_b64 v159, v[154:155]
.LBB0_944:
	s_or_b64 exec, exec, s[4:5]
	v_add_u32_e32 v156, 0x90, v177
	v_add_u32_e32 v154, s69, v156
	v_mov_b32_e32 v155, v153
	s_waitcnt lgkmcnt(0)
	v_lshlrev_b64 v[158:159], 12, v[154:155]
	v_lshl_add_u64 v[158:159], s[22:23], 0, v[158:159]
	v_lshl_add_u64 v[166:167], v[162:163], 1, v[158:159]
	s_mov_b32 s98, 0xb0000
	s_mov_b32 s99, 0
	v_lshl_add_u64 v[230:231], v[248:249], 0, s[98:99]
	global_load_dwordx4 v[226:229], v[230:231], off
	global_load_dwordx4 v[230:233], v[230:231], off offset:256
	s_waitcnt vmcnt(9)
	v_mov_b32_e32 v158, v234
	v_mov_b32_e32 v159, v235
	v_mov_b32_e32 v160, v236
	v_mov_b32_e32 v161, v237
	v_lshlrev_b32_e32 v182, 16, v158
	v_and_b32_e32 v183, 0xffff0000, v158
	v_lshlrev_b32_e32 v158, 16, v159
	v_and_b32_e32 v159, 0xffff0000, v159
	v_lshlrev_b32_e32 v184, 16, v160
	v_and_b32_e32 v185, 0xffff0000, v160
	v_lshlrev_b32_e32 v160, 16, v161
	v_and_b32_e32 v161, 0xffff0000, v161
	s_waitcnt vmcnt(8)
	v_mov_b32_e32 v178, v238
	v_mov_b32_e32 v179, v239
	v_mov_b32_e32 v180, v240
	v_mov_b32_e32 v181, v241
	v_lshlrev_b32_e32 v186, 16, v178
	v_and_b32_e32 v187, 0xffff0000, v178
	v_lshlrev_b32_e32 v178, 16, v179
	v_and_b32_e32 v179, 0xffff0000, v179
	v_lshlrev_b32_e32 v188, 16, v180
	v_and_b32_e32 v189, 0xffff0000, v180
	v_lshlrev_b32_e32 v180, 16, v181
	v_and_b32_e32 v181, 0xffff0000, v181
	v_pk_fma_f32 v[80:81], v[80:81], s[0:1], v[158:159] op_sel_hi:[1,0,1]
	v_pk_fma_f32 v[78:79], v[78:79], s[0:1], v[182:183] op_sel_hi:[1,0,1]
	v_pk_fma_f32 v[76:77], v[76:77], s[0:1], v[160:161] op_sel_hi:[1,0,1]
	v_pk_fma_f32 v[74:75], v[74:75], s[0:1], v[184:185] op_sel_hi:[1,0,1]
	v_pk_fma_f32 v[72:73], v[72:73], s[0:1], v[178:179] op_sel_hi:[1,0,1]
	v_pk_fma_f32 v[70:71], v[70:71], s[0:1], v[186:187] op_sel_hi:[1,0,1]
	v_pk_fma_f32 v[68:69], v[68:69], s[0:1], v[180:181] op_sel_hi:[1,0,1]
	v_mul_f32_e32 v157, v79, v79
	v_mul_f32_e32 v161, v81, v81
	v_pk_mul_f32 v[178:179], v[16:17], v[80:81]
	v_mul_f32_e32 v176, v75, v75
	v_mul_f32_e32 v194, v77, v77
	v_pk_mul_f32 v[182:183], v[12:13], v[76:77]
	v_pk_fma_f32 v[66:67], v[66:67], s[0:1], v[188:189] op_sel_hi:[1,0,1]
	v_pk_mul_f32 v[180:181], v[14:15], v[78:79]
	v_pk_mul_f32 v[184:185], v[10:11], v[74:75]
	v_mul_f32_e32 v195, v71, v71
	v_mul_f32_e32 v196, v73, v73
	v_pk_mul_f32 v[186:187], v[8:9], v[72:73]
	v_pk_mul_f32 v[190:191], v[4:5], v[68:69]
	v_fmac_f32_e32 v157, v78, v78
	v_fmac_f32_e32 v161, v80, v80
	v_max_f32_e64 v178, |v178|, |v179|
	v_fmac_f32_e32 v176, v74, v74
	v_fmac_f32_e32 v194, v76, v76
	v_max_f32_e64 v179, |v182|, |v183|
	v_pk_mul_f32 v[188:189], v[6:7], v[70:71]
	v_mul_f32_e32 v197, v67, v67
	v_mul_f32_e32 v198, v69, v69
	v_pk_mul_f32 v[192:193], v[2:3], v[66:67]
	v_fmac_f32_e32 v195, v70, v70
	v_fmac_f32_e32 v196, v72, v72
	v_max_f32_e64 v182, |v186|, |v187|
	v_max_f32_e64 v183, |v190|, |v191|
	v_add_f32_e32 v157, v157, v161
	v_max3_f32 v161, |v180|, |v181|, v178
	v_add_f32_e32 v176, v176, v194
	v_max3_f32 v178, |v184|, |v185|, v179
	v_fmac_f32_e32 v197, v66, v66
	v_fmac_f32_e32 v198, v68, v68
	v_add_f32_e32 v179, v195, v196
	v_max3_f32 v180, |v188|, |v189|, v182
	v_max3_f32 v182, |v192|, |v193|, v183
	v_add_f32_e32 v157, v157, v176
	v_max3_f32 v161, v161, 0, v178
	v_add_f32_e32 v181, v197, v198
	v_add_f32_e32 v157, v157, v179
	v_max3_f32 v176, v161, v180, v182
	v_add_f32_e32 v157, v157, v181
	ds_bpermute_b32 v179, v169, v176
	ds_bpermute_b32 v180, v169, v157
	v_cvt_pk_bf16_f32 v158, v78, v79
	v_cvt_pk_bf16_f32 v159, v80, v81
	v_cvt_pk_bf16_f32 v160, v74, v75
	v_cvt_pk_bf16_f32 v161, v76, v77
	global_store_dwordx4 v[166:167], v[158:161], off
	v_cvt_pk_bf16_f32 v178, v70, v71
	v_cvt_pk_bf16_f32 v181, v68, v69
	s_waitcnt lgkmcnt(1)
	v_max_f32_e32 v159, v179, v179
	s_waitcnt lgkmcnt(0)
	v_add_f32_e32 v158, v157, v180
	v_max_f32_e32 v157, v176, v159
	ds_bpermute_b32 v159, v168, v158
	ds_bpermute_b32 v160, v168, v157
	v_cvt_pk_bf16_f32 v179, v72, v73
	v_cvt_pk_bf16_f32 v180, v66, v67
	global_store_dwordx4 v[166:167], v[178:181], off offset:256
	s_and_saveexec_b64 s[0:1], s[2:3]
	s_cbranch_execz .LBB0_946
	v_lshl_add_u32 v161, v156, 5, s6
	s_waitcnt lgkmcnt(1)
	v_add_f32_e32 v156, v158, v159
	s_waitcnt lgkmcnt(0)
	v_max_f32_e32 v158, v160, v160
	v_max_f32_e32 v157, v157, v157
	v_max_f32_e32 v157, v157, v158
	ds_write_b64 v161, v[156:157]
.LBB0_946:
	s_or_b64 exec, exec, s[0:1]
	v_add_u32_e32 v158, 0xa0, v177
	v_add_u32_e32 v156, s69, v158
	v_mov_b32_e32 v157, 0
	s_waitcnt lgkmcnt(0)
	v_lshlrev_b64 v[160:161], 12, v[156:157]
	v_lshl_add_u64 v[160:161], s[22:23], 0, v[160:161]
	v_lshl_add_u64 v[186:187], v[162:163], 1, v[160:161]
	s_brev_b32 s0, 60
	s_waitcnt vmcnt(7)
	v_mov_b32_e32 v178, v218
	v_mov_b32_e32 v179, v219
	v_mov_b32_e32 v180, v220
	v_mov_b32_e32 v181, v221
	v_lshlrev_b32_e32 v160, 16, v178
	v_and_b32_e32 v161, 0xffff0000, v178
	v_lshlrev_b32_e32 v166, 16, v179
	v_and_b32_e32 v167, 0xffff0000, v179
	v_lshlrev_b32_e32 v178, 16, v180
	v_and_b32_e32 v179, 0xffff0000, v180
	v_lshlrev_b32_e32 v180, 16, v181
	v_and_b32_e32 v181, 0xffff0000, v181
	s_waitcnt vmcnt(6)
	v_mov_b32_e32 v182, v222
	v_mov_b32_e32 v183, v223
	v_mov_b32_e32 v184, v224
	v_mov_b32_e32 v185, v225
	v_lshlrev_b32_e32 v188, 16, v182
	v_and_b32_e32 v189, 0xffff0000, v182
	v_lshlrev_b32_e32 v182, 16, v183
	v_and_b32_e32 v183, 0xffff0000, v183
	v_lshlrev_b32_e32 v190, 16, v184
	v_and_b32_e32 v191, 0xffff0000, v184
	v_lshlrev_b32_e32 v184, 16, v185
	v_and_b32_e32 v185, 0xffff0000, v185
	v_pk_fma_f32 v[64:65], v[64:65], s[0:1], v[166:167] op_sel_hi:[1,0,1]
	v_pk_fma_f32 v[62:63], v[62:63], s[0:1], v[160:161] op_sel_hi:[1,0,1]
	v_pk_fma_f32 v[60:61], v[60:61], s[0:1], v[180:181] op_sel_hi:[1,0,1]
	v_pk_fma_f32 v[58:59], v[58:59], s[0:1], v[178:179] op_sel_hi:[1,0,1]
	v_pk_fma_f32 v[56:57], v[56:57], s[0:1], v[182:183] op_sel_hi:[1,0,1]
	v_pk_fma_f32 v[54:55], v[54:55], s[0:1], v[188:189] op_sel_hi:[1,0,1]
	v_pk_fma_f32 v[52:53], v[52:53], s[0:1], v[184:185] op_sel_hi:[1,0,1]
	v_mul_f32_e32 v159, v63, v63
	v_mul_f32_e32 v176, v65, v65
	v_pk_mul_f32 v[160:161], v[16:17], v[64:65]
	v_mul_f32_e32 v181, v59, v59
	v_mul_f32_e32 v196, v61, v61
	v_pk_mul_f32 v[182:183], v[12:13], v[60:61]
	v_pk_fma_f32 v[50:51], v[50:51], s[0:1], v[190:191] op_sel_hi:[1,0,1]
	v_pk_mul_f32 v[166:167], v[14:15], v[62:63]
	v_pk_mul_f32 v[184:185], v[10:11], v[58:59]
	v_mul_f32_e32 v197, v55, v55
	v_mul_f32_e32 v198, v57, v57
	v_pk_mul_f32 v[188:189], v[8:9], v[56:57]
	v_pk_mul_f32 v[192:193], v[4:5], v[52:53]
	v_fmac_f32_e32 v159, v62, v62
	v_fmac_f32_e32 v176, v64, v64
	v_max_f32_e64 v160, |v160|, |v161|
	v_fmac_f32_e32 v181, v58, v58
	v_fmac_f32_e32 v196, v60, v60
	v_max_f32_e64 v161, |v182|, |v183|
	v_pk_mul_f32 v[190:191], v[6:7], v[54:55]
	v_mul_f32_e32 v199, v51, v51
	v_mul_f32_e32 v201, v53, v53
	v_pk_mul_f32 v[194:195], v[2:3], v[50:51]
	v_fmac_f32_e32 v197, v54, v54
	v_fmac_f32_e32 v198, v56, v56
	v_max_f32_e64 v182, |v188|, |v189|
	v_max_f32_e64 v183, |v192|, |v193|
	v_add_f32_e32 v159, v159, v176
	v_max3_f32 v160, |v166|, |v167|, v160
	v_add_f32_e32 v166, v181, v196
	v_max3_f32 v161, |v184|, |v185|, v161
	v_fmac_f32_e32 v199, v50, v50
	v_fmac_f32_e32 v201, v52, v52
	v_add_f32_e32 v167, v197, v198
	v_max3_f32 v176, |v190|, |v191|, v182
	v_max3_f32 v182, |v194|, |v195|, v183
	v_add_f32_e32 v159, v159, v166
	v_max3_f32 v160, v160, 0, v161
	v_add_f32_e32 v181, v199, v201
	v_add_f32_e32 v159, v159, v167
	v_max3_f32 v161, v160, v176, v182
	v_add_f32_e32 v159, v159, v181
	ds_bpermute_b32 v160, v169, v161
	ds_bpermute_b32 v166, v169, v159
	v_cvt_pk_bf16_f32 v178, v62, v63
	v_cvt_pk_bf16_f32 v179, v64, v65
	v_cvt_pk_bf16_f32 v180, v58, v59
	s_waitcnt lgkmcnt(1)
	v_max_f32_e32 v167, v160, v160
	s_waitcnt lgkmcnt(0)
	v_add_f32_e32 v160, v159, v166
	v_max_f32_e32 v159, v161, v167
	ds_bpermute_b32 v161, v168, v160
	ds_bpermute_b32 v166, v168, v159
	v_cvt_pk_bf16_f32 v181, v60, v61
	v_cvt_pk_bf16_f32 v182, v54, v55
	v_cvt_pk_bf16_f32 v183, v56, v57
	v_cvt_pk_bf16_f32 v184, v50, v51
	v_cvt_pk_bf16_f32 v185, v52, v53
	global_store_dwordx4 v[186:187], v[178:181], off
	global_store_dwordx4 v[186:187], v[182:185], off offset:256
	s_and_saveexec_b64 s[4:5], s[2:3]
	s_cbranch_execz .LBB0_948
	v_lshl_add_u32 v167, v158, 5, s6
	s_waitcnt lgkmcnt(1)
	v_add_f32_e32 v158, v160, v161
	s_waitcnt lgkmcnt(0)
	v_max_f32_e32 v160, v166, v166
	v_max_f32_e32 v159, v159, v159
	v_max_f32_e32 v159, v159, v160
	ds_write_b64 v167, v[158:159]
.LBB0_948:
	s_or_b64 exec, exec, s[4:5]
	v_add_u32_e32 v160, 0xb0, v177
	v_add_u32_e32 v158, s69, v160
	v_mov_b32_e32 v159, v157
	s_waitcnt lgkmcnt(0)
	v_lshlrev_b64 v[166:167], 12, v[158:159]
	v_lshl_add_u64 v[166:167], s[22:23], 0, v[166:167]
	v_lshl_add_u64 v[186:187], v[162:163], 1, v[166:167]
	s_waitcnt vmcnt(5)
	v_mov_b32_e32 v178, v226
	v_mov_b32_e32 v179, v227
	v_mov_b32_e32 v180, v228
	v_mov_b32_e32 v181, v229
	v_lshlrev_b32_e32 v166, 16, v178
	v_and_b32_e32 v167, 0xffff0000, v178
	v_lshlrev_b32_e32 v178, 16, v179
	v_and_b32_e32 v179, 0xffff0000, v179
	v_lshlrev_b32_e32 v188, 16, v180
	v_and_b32_e32 v189, 0xffff0000, v180
	v_lshlrev_b32_e32 v180, 16, v181
	v_and_b32_e32 v181, 0xffff0000, v181
	s_waitcnt vmcnt(4)
	v_mov_b32_e32 v182, v230
	v_mov_b32_e32 v183, v231
	v_mov_b32_e32 v184, v232
	v_mov_b32_e32 v185, v233
	v_lshlrev_b32_e32 v190, 16, v182
	v_and_b32_e32 v191, 0xffff0000, v182
	v_lshlrev_b32_e32 v182, 16, v183
	v_and_b32_e32 v183, 0xffff0000, v183
	v_lshlrev_b32_e32 v192, 16, v184
	v_and_b32_e32 v193, 0xffff0000, v184
	v_lshlrev_b32_e32 v184, 16, v185
	v_and_b32_e32 v185, 0xffff0000, v185
	v_pk_fma_f32 v[48:49], v[48:49], s[0:1], v[178:179] op_sel_hi:[1,0,1]
	v_pk_fma_f32 v[46:47], v[46:47], s[0:1], v[166:167] op_sel_hi:[1,0,1]
	v_pk_fma_f32 v[44:45], v[44:45], s[0:1], v[180:181] op_sel_hi:[1,0,1]
	v_pk_fma_f32 v[42:43], v[42:43], s[0:1], v[188:189] op_sel_hi:[1,0,1]
	v_pk_fma_f32 v[40:41], v[40:41], s[0:1], v[182:183] op_sel_hi:[1,0,1]
	v_pk_fma_f32 v[38:39], v[38:39], s[0:1], v[190:191] op_sel_hi:[1,0,1]
	v_pk_fma_f32 v[36:37], v[36:37], s[0:1], v[184:185] op_sel_hi:[1,0,1]
	v_mul_f32_e32 v161, v47, v47
	v_mul_f32_e32 v176, v49, v49
	v_pk_mul_f32 v[166:167], v[16:17], v[48:49]
	v_mul_f32_e32 v181, v43, v43
	v_mul_f32_e32 v198, v45, v45
	v_pk_mul_f32 v[184:185], v[12:13], v[44:45]
	v_pk_fma_f32 v[34:35], v[34:35], s[0:1], v[192:193] op_sel_hi:[1,0,1]
	v_pk_mul_f32 v[182:183], v[14:15], v[46:47]
	v_pk_mul_f32 v[188:189], v[10:11], v[42:43]
	v_mul_f32_e32 v199, v39, v39
	v_mul_f32_e32 v201, v41, v41
	v_pk_mul_f32 v[190:191], v[8:9], v[40:41]
	v_pk_mul_f32 v[194:195], v[4:5], v[36:37]
	v_fmac_f32_e32 v161, v46, v46
	v_fmac_f32_e32 v176, v48, v48
	v_max_f32_e64 v166, |v166|, |v167|
	v_fmac_f32_e32 v181, v42, v42
	v_fmac_f32_e32 v198, v44, v44
	v_max_f32_e64 v167, |v184|, |v185|
	v_pk_mul_f32 v[192:193], v[6:7], v[38:39]
	v_mul_f32_e32 v202, v35, v35
	v_mul_f32_e32 v203, v37, v37
	v_pk_mul_f32 v[196:197], v[2:3], v[34:35]
	v_fmac_f32_e32 v199, v38, v38
	v_fmac_f32_e32 v201, v40, v40
	v_max_f32_e64 v184, |v190|, |v191|
	v_max_f32_e64 v185, |v194|, |v195|
	v_add_f32_e32 v161, v161, v176
	v_max3_f32 v166, |v182|, |v183|, v166
	v_add_f32_e32 v176, v181, v198
	v_max3_f32 v167, |v188|, |v189|, v167
	v_fmac_f32_e32 v202, v34, v34
	v_fmac_f32_e32 v203, v36, v36
	v_add_f32_e32 v181, v199, v201
	v_max3_f32 v182, |v192|, |v193|, v184
	v_max3_f32 v184, |v196|, |v197|, v185
	v_add_f32_e32 v161, v161, v176
	v_max3_f32 v166, v166, 0, v167
	v_add_f32_e32 v183, v202, v203
	v_add_f32_e32 v161, v161, v181
	v_max3_f32 v167, v166, v182, v184
	v_add_f32_e32 v161, v161, v183
	ds_bpermute_b32 v166, v169, v167
	ds_bpermute_b32 v176, v169, v161
	v_cvt_pk_bf16_f32 v178, v46, v47
	v_cvt_pk_bf16_f32 v179, v48, v49
	v_cvt_pk_bf16_f32 v180, v42, v43
	v_cvt_pk_bf16_f32 v181, v44, v45
	global_store_dwordx4 v[186:187], v[178:181], off
	v_cvt_pk_bf16_f32 v182, v38, v39
	v_cvt_pk_bf16_f32 v183, v40, v41
	s_waitcnt lgkmcnt(1)
	v_max_f32_e32 v178, v166, v166
	s_waitcnt lgkmcnt(0)
	v_add_f32_e32 v166, v161, v176
	v_max_f32_e32 v161, v167, v178
	ds_bpermute_b32 v167, v168, v166
	ds_bpermute_b32 v176, v168, v161
	v_cvt_pk_bf16_f32 v184, v34, v35
	v_cvt_pk_bf16_f32 v185, v36, v37
	global_store_dwordx4 v[186:187], v[182:185], off offset:256
	s_and_saveexec_b64 s[0:1], s[2:3]
	s_cbranch_execz .LBB0_950
	v_lshl_add_u32 v178, v160, 5, s6
	s_waitcnt lgkmcnt(1)
	v_add_f32_e32 v160, v166, v167
	s_waitcnt lgkmcnt(0)
	v_max_f32_e32 v166, v176, v176
	v_max_f32_e32 v161, v161, v161
	v_max_f32_e32 v161, v161, v166
	ds_write_b64 v178, v[160:161]

.LBB0_981:
	s_lshl_b32 s0, s44, 5
	s_lshl_b32 s10, s35, 8
	s_or_b32 s0, s0, s61
	v_add_u32_e32 v164, s10, v177
	v_mov_b32_e32 v165, 0
	v_or_b32_e32 v162, s0, v175
	v_lshlrev_b64 v[2:3], 12, v[164:165]
	v_ashrrev_i32_e32 v163, 31, v162
	v_lshl_add_u64 v[2:3], s[22:23], 0, v[2:3]
	s_nop 15
	s_nop 7
	v_lshl_add_u64 v[166:167], v[162:163], 1, v[2:3]
	s_waitcnt vmcnt(0)
	s_barrier
	global_load_dwordx4 v[18:21], v[166:167], off
	v_mov_b32_e32 v248, v166
	v_mov_b32_e32 v249, v167
	global_load_dwordx4 v[22:25], v[166:167], off offset:256
	v_lshl_add_u64 v[2:3], v[162:163], 2, s[18:19]
	global_load_dwordx4 v[14:17], v[2:3], off
	global_load_dwordx4 v[10:13], v[2:3], off offset:16
	global_load_dwordx4 v[6:9], v[2:3], off offset:512
	s_nop 0
	global_load_dwordx4 v[2:5], v[2:3], off offset:528
	s_mov_b32 s98, 0x10000
	s_mov_b32 s99, 0
	v_lshl_add_u64 v[230:231], v[248:249], 0, s[98:99]
	global_load_dwordx4 v[226:229], v[230:231], off
	global_load_dwordx4 v[230:233], v[230:231], off offset:256
	s_mov_b32 s98, 0x20000
	s_mov_b32 s99, 0
	v_lshl_add_u64 v[238:239], v[248:249], 0, s[98:99]
	global_load_dwordx4 v[234:237], v[238:239], off
	global_load_dwordx4 v[238:241], v[238:239], off offset:256
	s_lshl_b32 s1, s44, 3
	s_brev_b32 s0, 60
	s_add_i32 s11, s1, 0
	s_waitcnt vmcnt(4)
	v_lshlrev_b32_e32 v26, 16, v18
	v_and_b32_e32 v27, 0xffff0000, v18
	v_lshlrev_b32_e32 v18, 16, v19
	v_and_b32_e32 v19, 0xffff0000, v19
	v_lshlrev_b32_e32 v170, 16, v20
	v_and_b32_e32 v171, 0xffff0000, v20
	v_lshlrev_b32_e32 v20, 16, v21
	v_and_b32_e32 v21, 0xffff0000, v21
	v_lshlrev_b32_e32 v172, 16, v22
	v_and_b32_e32 v173, 0xffff0000, v22
	v_lshlrev_b32_e32 v22, 16, v23
	v_and_b32_e32 v23, 0xffff0000, v23
	v_lshlrev_b32_e32 v174, 16, v24
	v_and_b32_e32 v175, 0xffff0000, v24
	v_lshlrev_b32_e32 v178, 16, v25
	v_and_b32_e32 v179, 0xffff0000, v25
	v_pk_fma_f32 v[32:33], v[148:149], s[0:1], v[18:19] op_sel_hi:[1,0,1]
	v_pk_fma_f32 v[30:31], v[146:147], s[0:1], v[26:27] op_sel_hi:[1,0,1]
	v_pk_fma_f32 v[28:29], v[152:153], s[0:1], v[20:21] op_sel_hi:[1,0,1]
	v_pk_fma_f32 v[26:27], v[150:151], s[0:1], v[170:171] op_sel_hi:[1,0,1]
	v_pk_fma_f32 v[24:25], v[156:157], s[0:1], v[22:23] op_sel_hi:[1,0,1]
	v_pk_fma_f32 v[22:23], v[154:155], s[0:1], v[172:173] op_sel_hi:[1,0,1]
	v_pk_fma_f32 v[20:21], v[160:161], s[0:1], v[178:179] op_sel_hi:[1,0,1]
	v_pk_fma_f32 v[18:19], v[158:159], s[0:1], v[174:175] op_sel_hi:[1,0,1]
	v_mul_f32_e32 v149, v31, v31
	v_mul_f32_e32 v174, v33, v33
	v_pk_mul_f32 v[150:151], v[16:17], v[32:33]
	v_mul_f32_e32 v175, v27, v27
	v_mul_f32_e32 v178, v29, v29
	v_pk_mul_f32 v[154:155], v[12:13], v[28:29]
	v_pk_mul_f32 v[152:153], v[14:15], v[30:31]
	v_pk_mul_f32 v[156:157], v[10:11], v[26:27]
	v_mul_f32_e32 v179, v23, v23
	v_mul_f32_e32 v180, v25, v25
	v_pk_mul_f32 v[158:159], v[8:9], v[24:25]
	v_pk_mul_f32 v[170:171], v[4:5], v[20:21]
	v_fmac_f32_e32 v149, v30, v30
	v_fmac_f32_e32 v174, v32, v32
	v_max_f32_e64 v150, |v150|, |v151|
	v_fmac_f32_e32 v175, v26, v26
	v_fmac_f32_e32 v178, v28, v28
	v_max_f32_e64 v151, |v154|, |v155|
	v_pk_mul_f32 v[160:161], v[6:7], v[22:23]
	v_mul_f32_e32 v181, v19, v19
	v_mul_f32_e32 v182, v21, v21
	v_pk_mul_f32 v[172:173], v[2:3], v[18:19]
	v_fmac_f32_e32 v179, v22, v22
	v_fmac_f32_e32 v180, v24, v24
	v_max_f32_e64 v154, |v158|, |v159|
	v_max_f32_e64 v155, |v170|, |v171|
	v_add_f32_e32 v149, v149, v174
	v_max3_f32 v150, |v152|, |v153|, v150
	v_add_f32_e32 v152, v175, v178
	v_max3_f32 v151, |v156|, |v157|, v151
	v_fmac_f32_e32 v181, v18, v18
	v_fmac_f32_e32 v182, v20, v20
	v_add_f32_e32 v153, v179, v180
	v_max3_f32 v154, |v160|, |v161|, v154
	v_max3_f32 v155, |v172|, |v173|, v155
	v_add_f32_e32 v149, v149, v152
	v_max3_f32 v150, v150, 0, v151
	v_add_f32_e32 v156, v181, v182
	v_add_f32_e32 v149, v149, v153
	v_max3_f32 v151, v150, v154, v155
	v_add_f32_e32 v152, v149, v156
	ds_bpermute_b32 v153, v169, v151
	ds_bpermute_b32 v154, v169, v152
	v_cvt_pk_bf16_f32 v146, v30, v31
	v_cvt_pk_bf16_f32 v147, v32, v33
	v_cvt_pk_bf16_f32 v148, v26, v27
	v_cvt_pk_bf16_f32 v149, v28, v29
	global_store_dwordx4 v[166:167], v[146:149], off
	v_cvt_pk_bf16_f32 v150, v22, v23
	s_waitcnt lgkmcnt(1)
	v_max_f32_e32 v146, v153, v153
	s_waitcnt lgkmcnt(0)
	v_add_f32_e32 v147, v152, v154
	v_max_f32_e32 v146, v151, v146
	ds_bpermute_b32 v148, v168, v147
	ds_bpermute_b32 v149, v168, v146
	v_cvt_pk_bf16_f32 v151, v24, v25
	v_cvt_pk_bf16_f32 v152, v18, v19
	v_cvt_pk_bf16_f32 v153, v20, v21
	global_store_dwordx4 v[166:167], v[150:153], off offset:256
	s_and_saveexec_b64 s[14:15], s[2:3]
	s_cbranch_execz .LBB0_983
	s_waitcnt lgkmcnt(1)
	v_add_f32_e32 v148, v147, v148
	s_waitcnt lgkmcnt(0)
	v_max_f32_e32 v147, v149, v149
	v_max_f32_e32 v146, v146, v146
	v_lshl_add_u32 v150, v177, 5, s11
	v_max_f32_e32 v149, v146, v147
	ds_write_b64 v150, v[148:149]
.LBB0_983:
	s_or_b64 exec, exec, s[14:15]
	s_waitcnt lgkmcnt(1)
	v_or_b32_e32 v148, 16, v177
	v_add_u32_e32 v146, s10, v148
	v_mov_b32_e32 v147, v165
	v_lshlrev_b64 v[150:151], 12, v[146:147]
	v_lshl_add_u64 v[150:151], s[22:23], 0, v[150:151]
	v_lshl_add_u64 v[158:159], v[162:163], 1, v[150:151]
	s_mov_b32 s98, 0x30000
	s_mov_b32 s99, 0
	v_lshl_add_u64 v[222:223], v[248:249], 0, s[98:99]
	global_load_dwordx4 v[218:221], v[222:223], off
	global_load_dwordx4 v[222:225], v[222:223], off offset:256
	s_waitcnt vmcnt(7)
	v_mov_b32_e32 v150, v226
	v_mov_b32_e32 v151, v227
	v_mov_b32_e32 v152, v228
	v_mov_b32_e32 v153, v229
	v_lshlrev_b32_e32 v160, 16, v150
	v_and_b32_e32 v161, 0xffff0000, v150
	v_lshlrev_b32_e32 v150, 16, v151
	v_and_b32_e32 v151, 0xffff0000, v151
	v_lshlrev_b32_e32 v166, 16, v152
	v_and_b32_e32 v167, 0xffff0000, v152
	v_lshlrev_b32_e32 v152, 16, v153
	v_and_b32_e32 v153, 0xffff0000, v153
	s_waitcnt vmcnt(6)
	v_mov_b32_e32 v154, v230
	v_mov_b32_e32 v155, v231
	v_mov_b32_e32 v156, v232
	v_mov_b32_e32 v157, v233
	v_lshlrev_b32_e32 v170, 16, v154
	v_and_b32_e32 v171, 0xffff0000, v154
	v_lshlrev_b32_e32 v154, 16, v155
	v_and_b32_e32 v155, 0xffff0000, v155
	v_lshlrev_b32_e32 v172, 16, v156
	v_and_b32_e32 v173, 0xffff0000, v156
	v_lshlrev_b32_e32 v156, 16, v157
	v_and_b32_e32 v157, 0xffff0000, v157
	v_pk_fma_f32 v[112:113], v[112:113], s[0:1], v[150:151] op_sel_hi:[1,0,1]
	v_pk_fma_f32 v[110:111], v[110:111], s[0:1], v[160:161] op_sel_hi:[1,0,1]
	v_pk_fma_f32 v[108:109], v[108:109], s[0:1], v[152:153] op_sel_hi:[1,0,1]
	v_pk_fma_f32 v[106:107], v[106:107], s[0:1], v[166:167] op_sel_hi:[1,0,1]
	v_pk_fma_f32 v[104:105], v[104:105], s[0:1], v[154:155] op_sel_hi:[1,0,1]
	v_pk_fma_f32 v[102:103], v[102:103], s[0:1], v[170:171] op_sel_hi:[1,0,1]
	v_pk_fma_f32 v[100:101], v[100:101], s[0:1], v[156:157] op_sel_hi:[1,0,1]
	s_waitcnt lgkmcnt(0)
	v_mul_f32_e32 v149, v111, v111
	v_mul_f32_e32 v153, v113, v113
	v_pk_mul_f32 v[154:155], v[16:17], v[112:113]
	v_mul_f32_e32 v180, v107, v107
	v_mul_f32_e32 v181, v109, v109
	v_pk_mul_f32 v[160:161], v[12:13], v[108:109]
	v_pk_fma_f32 v[98:99], v[98:99], s[0:1], v[172:173] op_sel_hi:[1,0,1]
	v_pk_mul_f32 v[156:157], v[14:15], v[110:111]
	v_pk_mul_f32 v[166:167], v[10:11], v[106:107]
	v_mul_f32_e32 v182, v103, v103
	v_mul_f32_e32 v183, v105, v105
	v_pk_mul_f32 v[170:171], v[8:9], v[104:105]
	v_pk_mul_f32 v[174:175], v[4:5], v[100:101]
	v_fmac_f32_e32 v149, v110, v110
	v_fmac_f32_e32 v153, v112, v112
	v_max_f32_e64 v154, |v154|, |v155|
	v_fmac_f32_e32 v180, v106, v106
	v_fmac_f32_e32 v181, v108, v108
	v_max_f32_e64 v155, |v160|, |v161|
	v_pk_mul_f32 v[172:173], v[6:7], v[102:103]
	v_mul_f32_e32 v184, v99, v99
	v_mul_f32_e32 v185, v101, v101
	v_pk_mul_f32 v[178:179], v[2:3], v[98:99]
	v_fmac_f32_e32 v182, v102, v102
	v_fmac_f32_e32 v183, v104, v104
	v_max_f32_e64 v160, |v170|, |v171|
	v_max_f32_e64 v161, |v174|, |v175|
	v_add_f32_e32 v149, v149, v153
	v_max3_f32 v153, |v156|, |v157|, v154
	v_add_f32_e32 v154, v180, v181
	v_max3_f32 v155, |v166|, |v167|, v155
	v_fmac_f32_e32 v184, v98, v98
	v_fmac_f32_e32 v185, v100, v100
	v_add_f32_e32 v156, v182, v183
	v_max3_f32 v157, |v172|, |v173|, v160
	v_max3_f32 v161, |v178|, |v179|, v161
	v_add_f32_e32 v149, v149, v154
	v_max3_f32 v153, v153, 0, v155
	v_add_f32_e32 v160, v184, v185
	v_add_f32_e32 v149, v149, v156
	v_max3_f32 v155, v153, v157, v161
	v_add_f32_e32 v149, v149, v160
	ds_bpermute_b32 v156, v169, v155
	ds_bpermute_b32 v157, v169, v149
	v_cvt_pk_bf16_f32 v150, v110, v111
	v_cvt_pk_bf16_f32 v151, v112, v113
	v_cvt_pk_bf16_f32 v152, v106, v107
	v_cvt_pk_bf16_f32 v153, v108, v109
	global_store_dwordx4 v[158:159], v[150:153], off
	v_cvt_pk_bf16_f32 v154, v102, v103
	s_waitcnt lgkmcnt(1)
	v_max_f32_e32 v151, v156, v156
	s_waitcnt lgkmcnt(0)
	v_add_f32_e32 v150, v149, v157
	v_max_f32_e32 v149, v155, v151
	ds_bpermute_b32 v151, v168, v150
	ds_bpermute_b32 v152, v168, v149
	v_cvt_pk_bf16_f32 v155, v104, v105
	v_cvt_pk_bf16_f32 v156, v98, v99
	v_cvt_pk_bf16_f32 v157, v100, v101
	global_store_dwordx4 v[158:159], v[154:157], off offset:256
	s_and_saveexec_b64 s[0:1], s[2:3]
	s_cbranch_execz .LBB0_985
	v_lshl_add_u32 v153, v148, 5, s11
	s_waitcnt lgkmcnt(1)
	v_add_f32_e32 v148, v150, v151
	s_waitcnt lgkmcnt(0)
	v_max_f32_e32 v150, v152, v152
	v_max_f32_e32 v149, v149, v149
	v_max_f32_e32 v149, v149, v150
	ds_write_b64 v153, v[148:149]
.LBB0_985:
	s_or_b64 exec, exec, s[0:1]
	v_or_b32_e32 v150, 32, v177
	v_add_u32_e32 v148, s10, v150
	v_mov_b32_e32 v149, 0
	s_waitcnt lgkmcnt(0)
	v_lshlrev_b64 v[152:153], 12, v[148:149]
	v_lshl_add_u64 v[152:153], s[22:23], 0, v[152:153]
	v_lshl_add_u64 v[160:161], v[162:163], 1, v[152:153]
	s_mov_b32 s98, 0x80000
	s_mov_b32 s99, 0
	v_lshl_add_u64 v[230:231], v[248:249], 0, s[98:99]
	global_load_dwordx4 v[226:229], v[230:231], off
	global_load_dwordx4 v[230:233], v[230:231], off offset:256
	s_brev_b32 s0, 60
	s_waitcnt vmcnt(9)
	v_mov_b32_e32 v152, v234
	v_mov_b32_e32 v153, v235
	v_mov_b32_e32 v154, v236
	v_mov_b32_e32 v155, v237
	v_lshlrev_b32_e32 v166, 16, v152
	v_and_b32_e32 v167, 0xffff0000, v152
	v_lshlrev_b32_e32 v152, 16, v153
	v_and_b32_e32 v153, 0xffff0000, v153
	v_lshlrev_b32_e32 v170, 16, v154
	v_and_b32_e32 v171, 0xffff0000, v154
	v_lshlrev_b32_e32 v154, 16, v155
	v_and_b32_e32 v155, 0xffff0000, v155
	s_waitcnt vmcnt(8)
	v_mov_b32_e32 v156, v238
	v_mov_b32_e32 v157, v239
	v_mov_b32_e32 v158, v240
	v_mov_b32_e32 v159, v241
	v_lshlrev_b32_e32 v172, 16, v156
	v_and_b32_e32 v173, 0xffff0000, v156
	v_lshlrev_b32_e32 v156, 16, v157
	v_and_b32_e32 v157, 0xffff0000, v157
	v_lshlrev_b32_e32 v174, 16, v158
	v_and_b32_e32 v175, 0xffff0000, v158
	v_lshlrev_b32_e32 v158, 16, v159
	v_and_b32_e32 v159, 0xffff0000, v159
	v_pk_fma_f32 v[144:145], v[144:145], s[0:1], v[152:153] op_sel_hi:[1,0,1]
	v_pk_fma_f32 v[142:143], v[142:143], s[0:1], v[166:167] op_sel_hi:[1,0,1]
	v_pk_fma_f32 v[140:141], v[140:141], s[0:1], v[154:155] op_sel_hi:[1,0,1]
	v_pk_fma_f32 v[138:139], v[138:139], s[0:1], v[170:171] op_sel_hi:[1,0,1]
	v_pk_fma_f32 v[136:137], v[136:137], s[0:1], v[156:157] op_sel_hi:[1,0,1]
	v_pk_fma_f32 v[134:135], v[134:135], s[0:1], v[172:173] op_sel_hi:[1,0,1]
	v_pk_fma_f32 v[132:133], v[132:133], s[0:1], v[158:159] op_sel_hi:[1,0,1]
	v_mul_f32_e32 v151, v143, v143
	v_mul_f32_e32 v155, v145, v145
	v_pk_mul_f32 v[156:157], v[16:17], v[144:145]
	v_mul_f32_e32 v182, v139, v139
	v_mul_f32_e32 v183, v141, v141
	v_pk_mul_f32 v[166:167], v[12:13], v[140:141]
	v_pk_fma_f32 v[130:131], v[130:131], s[0:1], v[174:175] op_sel_hi:[1,0,1]
	v_pk_mul_f32 v[158:159], v[14:15], v[142:143]
	v_pk_mul_f32 v[170:171], v[10:11], v[138:139]
	v_mul_f32_e32 v184, v135, v135
	v_mul_f32_e32 v185, v137, v137
	v_pk_mul_f32 v[172:173], v[8:9], v[136:137]
	v_pk_mul_f32 v[178:179], v[4:5], v[132:133]
	v_fmac_f32_e32 v151, v142, v142
	v_fmac_f32_e32 v155, v144, v144
	v_max_f32_e64 v156, |v156|, |v157|
	v_fmac_f32_e32 v182, v138, v138
	v_fmac_f32_e32 v183, v140, v140
	v_max_f32_e64 v157, |v166|, |v167|
	v_pk_mul_f32 v[174:175], v[6:7], v[134:135]
	v_mul_f32_e32 v186, v131, v131
	v_mul_f32_e32 v187, v133, v133
	v_pk_mul_f32 v[180:181], v[2:3], v[130:131]
	v_fmac_f32_e32 v184, v134, v134
	v_fmac_f32_e32 v185, v136, v136
	v_max_f32_e64 v166, |v172|, |v173|
	v_max_f32_e64 v167, |v178|, |v179|
	v_add_f32_e32 v151, v151, v155
	v_max3_f32 v155, |v158|, |v159|, v156
	v_add_f32_e32 v156, v182, v183
	v_max3_f32 v157, |v170|, |v171|, v157
	v_fmac_f32_e32 v186, v130, v130
	v_fmac_f32_e32 v187, v132, v132
	v_add_f32_e32 v158, v184, v185
	v_max3_f32 v159, |v174|, |v175|, v166
	v_max3_f32 v167, |v180|, |v181|, v167
	v_add_f32_e32 v151, v151, v156
	v_max3_f32 v155, v155, 0, v157
	v_add_f32_e32 v166, v186, v187
	v_add_f32_e32 v151, v151, v158
	v_max3_f32 v157, v155, v159, v167
	v_add_f32_e32 v151, v151, v166
	ds_bpermute_b32 v158, v169, v157
	ds_bpermute_b32 v159, v169, v151
	v_cvt_pk_bf16_f32 v152, v142, v143
	v_cvt_pk_bf16_f32 v153, v144, v145
	v_cvt_pk_bf16_f32 v154, v138, v139
	v_cvt_pk_bf16_f32 v155, v140, v141
	global_store_dwordx4 v[160:161], v[152:155], off
	v_cvt_pk_bf16_f32 v156, v134, v135
	s_waitcnt lgkmcnt(1)
	v_max_f32_e32 v153, v158, v158
	s_waitcnt lgkmcnt(0)
	v_add_f32_e32 v152, v151, v159
	v_max_f32_e32 v151, v157, v153
	ds_bpermute_b32 v153, v168, v152
	ds_bpermute_b32 v154, v168, v151
	v_cvt_pk_bf16_f32 v157, v136, v137
	v_cvt_pk_bf16_f32 v158, v130, v131
	v_cvt_pk_bf16_f32 v159, v132, v133
	global_store_dwordx4 v[160:161], v[156:159], off offset:256
	s_and_saveexec_b64 s[14:15], s[2:3]
	s_cbranch_execz .LBB0_987
	v_lshl_add_u32 v155, v150, 5, s11
	s_waitcnt lgkmcnt(1)
	v_add_f32_e32 v150, v152, v153
	s_waitcnt lgkmcnt(0)
	v_max_f32_e32 v152, v154, v154
	v_max_f32_e32 v151, v151, v151
	v_max_f32_e32 v151, v151, v152
	ds_write_b64 v155, v[150:151]
.LBB0_987:
	s_or_b64 exec, exec, s[14:15]
	v_or_b32_e32 v152, 48, v177
	v_add_u32_e32 v150, s10, v152
	v_mov_b32_e32 v151, v149
	s_waitcnt lgkmcnt(0)
	v_lshlrev_b64 v[154:155], 12, v[150:151]
	v_lshl_add_u64 v[154:155], s[22:23], 0, v[154:155]
	v_lshl_add_u64 v[166:167], v[162:163], 1, v[154:155]
	s_mov_b32 s98, 0x90000
	s_mov_b32 s99, 0
	v_lshl_add_u64 v[238:239], v[248:249], 0, s[98:99]
	global_load_dwordx4 v[234:237], v[238:239], off
	global_load_dwordx4 v[238:241], v[238:239], off offset:256
	s_waitcnt vmcnt(9)
	v_mov_b32_e32 v154, v218
	v_mov_b32_e32 v155, v219
	v_mov_b32_e32 v156, v220
	v_mov_b32_e32 v157, v221
	v_lshlrev_b32_e32 v170, 16, v154
	v_and_b32_e32 v171, 0xffff0000, v154
	v_lshlrev_b32_e32 v154, 16, v155
	v_and_b32_e32 v155, 0xffff0000, v155
	v_lshlrev_b32_e32 v172, 16, v156
	v_and_b32_e32 v173, 0xffff0000, v156
	v_lshlrev_b32_e32 v156, 16, v157
	v_and_b32_e32 v157, 0xffff0000, v157
	s_waitcnt vmcnt(8)
	v_mov_b32_e32 v158, v222
	v_mov_b32_e32 v159, v223
	v_mov_b32_e32 v160, v224
	v_mov_b32_e32 v161, v225
	v_lshlrev_b32_e32 v174, 16, v158
	v_and_b32_e32 v175, 0xffff0000, v158
	v_lshlrev_b32_e32 v158, 16, v159
	v_and_b32_e32 v159, 0xffff0000, v159
	v_lshlrev_b32_e32 v178, 16, v160
	v_and_b32_e32 v179, 0xffff0000, v160
	v_lshlrev_b32_e32 v160, 16, v161
	v_and_b32_e32 v161, 0xffff0000, v161
	v_pk_fma_f32 v[128:129], v[128:129], s[0:1], v[154:155] op_sel_hi:[1,0,1]
	v_pk_fma_f32 v[126:127], v[126:127], s[0:1], v[170:171] op_sel_hi:[1,0,1]
	v_pk_fma_f32 v[124:125], v[124:125], s[0:1], v[156:157] op_sel_hi:[1,0,1]
	v_pk_fma_f32 v[122:123], v[122:123], s[0:1], v[172:173] op_sel_hi:[1,0,1]
	v_pk_fma_f32 v[120:121], v[120:121], s[0:1], v[158:159] op_sel_hi:[1,0,1]
	v_pk_fma_f32 v[118:119], v[118:119], s[0:1], v[174:175] op_sel_hi:[1,0,1]
	v_pk_fma_f32 v[116:117], v[116:117], s[0:1], v[160:161] op_sel_hi:[1,0,1]
	v_mul_f32_e32 v153, v127, v127
	v_mul_f32_e32 v157, v129, v129
	v_pk_mul_f32 v[158:159], v[16:17], v[128:129]
	v_mul_f32_e32 v184, v123, v123
	v_mul_f32_e32 v185, v125, v125
	v_pk_mul_f32 v[170:171], v[12:13], v[124:125]
	v_pk_fma_f32 v[114:115], v[114:115], s[0:1], v[178:179] op_sel_hi:[1,0,1]
	v_pk_mul_f32 v[160:161], v[14:15], v[126:127]
	v_pk_mul_f32 v[172:173], v[10:11], v[122:123]
	v_mul_f32_e32 v186, v119, v119
	v_mul_f32_e32 v187, v121, v121
	v_pk_mul_f32 v[174:175], v[8:9], v[120:121]
	v_pk_mul_f32 v[180:181], v[4:5], v[116:117]
	v_fmac_f32_e32 v153, v126, v126
	v_fmac_f32_e32 v157, v128, v128
	v_max_f32_e64 v158, |v158|, |v159|
	v_fmac_f32_e32 v184, v122, v122
	v_fmac_f32_e32 v185, v124, v124
	v_max_f32_e64 v159, |v170|, |v171|
	v_pk_mul_f32 v[178:179], v[6:7], v[118:119]
	v_mul_f32_e32 v188, v115, v115
	v_mul_f32_e32 v189, v117, v117
	v_pk_mul_f32 v[182:183], v[2:3], v[114:115]
	v_fmac_f32_e32 v186, v118, v118
	v_fmac_f32_e32 v187, v120, v120
	v_max_f32_e64 v170, |v174|, |v175|
	v_max_f32_e64 v171, |v180|, |v181|
	v_add_f32_e32 v153, v153, v157
	v_max3_f32 v157, |v160|, |v161|, v158
	v_add_f32_e32 v158, v184, v185
	v_max3_f32 v159, |v172|, |v173|, v159
	v_fmac_f32_e32 v188, v114, v114
	v_fmac_f32_e32 v189, v116, v116
	v_add_f32_e32 v160, v186, v187
	v_max3_f32 v161, |v178|, |v179|, v170
	v_max3_f32 v171, |v182|, |v183|, v171
	v_add_f32_e32 v153, v153, v158
	v_max3_f32 v157, v157, 0, v159
	v_add_f32_e32 v170, v188, v189
	v_add_f32_e32 v153, v153, v160
	v_max3_f32 v159, v157, v161, v171
	v_add_f32_e32 v153, v153, v170
	ds_bpermute_b32 v160, v169, v159
	ds_bpermute_b32 v161, v169, v153
	v_cvt_pk_bf16_f32 v154, v126, v127
	v_cvt_pk_bf16_f32 v155, v128, v129
	v_cvt_pk_bf16_f32 v156, v122, v123
	v_cvt_pk_bf16_f32 v157, v124, v125
	global_store_dwordx4 v[166:167], v[154:157], off
	v_cvt_pk_bf16_f32 v158, v118, v119
	s_waitcnt lgkmcnt(1)
	v_max_f32_e32 v155, v160, v160
	s_waitcnt lgkmcnt(0)
	v_add_f32_e32 v154, v153, v161
	v_max_f32_e32 v153, v159, v155
	ds_bpermute_b32 v155, v168, v154
	ds_bpermute_b32 v156, v168, v153
	v_cvt_pk_bf16_f32 v159, v120, v121
	v_cvt_pk_bf16_f32 v160, v114, v115
	v_cvt_pk_bf16_f32 v161, v116, v117
	global_store_dwordx4 v[166:167], v[158:161], off offset:256
	s_and_saveexec_b64 s[0:1], s[2:3]
	s_cbranch_execz .LBB0_989
	v_lshl_add_u32 v157, v152, 5, s11
	s_waitcnt lgkmcnt(1)
	v_add_f32_e32 v152, v154, v155
	s_waitcnt lgkmcnt(0)
	v_max_f32_e32 v154, v156, v156
	v_max_f32_e32 v153, v153, v153
	v_max_f32_e32 v153, v153, v154
	ds_write_b64 v157, v[152:153]
.LBB0_989:
	s_or_b64 exec, exec, s[0:1]
	v_add_u32_e32 v154, 0x80, v177
	v_add_u32_e32 v152, s10, v154
	v_mov_b32_e32 v153, 0
	s_waitcnt lgkmcnt(0)
	v_lshlrev_b64 v[156:157], 12, v[152:153]
	v_lshl_add_u64 v[156:157], s[22:23], 0, v[156:157]
	v_lshl_add_u64 v[160:161], v[162:163], 1, v[156:157]
	s_mov_b32 s98, 0xa0000
	s_mov_b32 s99, 0
	v_lshl_add_u64 v[222:223], v[248:249], 0, s[98:99]
	global_load_dwordx4 v[218:221], v[222:223], off
	global_load_dwordx4 v[222:225], v[222:223], off offset:256
	s_brev_b32 s0, 60
	s_waitcnt vmcnt(9)
	v_mov_b32_e32 v156, v226
	v_mov_b32_e32 v157, v227
	v_mov_b32_e32 v158, v228
	v_mov_b32_e32 v159, v229
	v_lshlrev_b32_e32 v166, 16, v156
	v_and_b32_e32 v167, 0xffff0000, v156
	v_lshlrev_b32_e32 v156, 16, v157
	v_and_b32_e32 v157, 0xffff0000, v157
	v_lshlrev_b32_e32 v174, 16, v158
	v_and_b32_e32 v175, 0xffff0000, v158
	v_lshlrev_b32_e32 v158, 16, v159
	v_and_b32_e32 v159, 0xffff0000, v159
	s_waitcnt vmcnt(8)
	v_mov_b32_e32 v170, v230
	v_mov_b32_e32 v171, v231
	v_mov_b32_e32 v172, v232
	v_mov_b32_e32 v173, v233
	v_lshlrev_b32_e32 v178, 16, v170
	v_and_b32_e32 v179, 0xffff0000, v170
	v_lshlrev_b32_e32 v170, 16, v171
	v_and_b32_e32 v171, 0xffff0000, v171
	v_lshlrev_b32_e32 v180, 16, v172
	v_and_b32_e32 v181, 0xffff0000, v172
	v_lshlrev_b32_e32 v172, 16, v173
	v_and_b32_e32 v173, 0xffff0000, v173
	v_pk_fma_f32 v[96:97], v[96:97], s[0:1], v[156:157] op_sel_hi:[1,0,1]
	v_pk_fma_f32 v[94:95], v[94:95], s[0:1], v[166:167] op_sel_hi:[1,0,1]
	v_pk_fma_f32 v[92:93], v[92:93], s[0:1], v[158:159] op_sel_hi:[1,0,1]
	v_pk_fma_f32 v[90:91], v[90:91], s[0:1], v[174:175] op_sel_hi:[1,0,1]
	v_pk_fma_f32 v[88:89], v[88:89], s[0:1], v[170:171] op_sel_hi:[1,0,1]
	v_pk_fma_f32 v[86:87], v[86:87], s[0:1], v[178:179] op_sel_hi:[1,0,1]
	v_pk_fma_f32 v[84:85], v[84:85], s[0:1], v[172:173] op_sel_hi:[1,0,1]
	v_mul_f32_e32 v155, v95, v95
	v_mul_f32_e32 v159, v97, v97
	v_pk_mul_f32 v[166:167], v[16:17], v[96:97]
	v_mul_f32_e32 v186, v91, v91
	v_mul_f32_e32 v187, v93, v93
	v_pk_mul_f32 v[172:173], v[12:13], v[92:93]
	v_pk_fma_f32 v[82:83], v[82:83], s[0:1], v[180:181] op_sel_hi:[1,0,1]
	v_pk_mul_f32 v[170:171], v[14:15], v[94:95]
	v_pk_mul_f32 v[174:175], v[10:11], v[90:91]
	v_mul_f32_e32 v188, v87, v87
	v_mul_f32_e32 v189, v89, v89
	v_pk_mul_f32 v[178:179], v[8:9], v[88:89]
	v_pk_mul_f32 v[182:183], v[4:5], v[84:85]
	v_fmac_f32_e32 v155, v94, v94
	v_fmac_f32_e32 v159, v96, v96
	v_max_f32_e64 v166, |v166|, |v167|
	v_fmac_f32_e32 v186, v90, v90
	v_fmac_f32_e32 v187, v92, v92
	v_max_f32_e64 v167, |v172|, |v173|
	v_pk_mul_f32 v[180:181], v[6:7], v[86:87]
	v_mul_f32_e32 v190, v83, v83
	v_mul_f32_e32 v191, v85, v85
	v_pk_mul_f32 v[184:185], v[2:3], v[82:83]
	v_fmac_f32_e32 v188, v86, v86
	v_fmac_f32_e32 v189, v88, v88
	v_max_f32_e64 v172, |v178|, |v179|
	v_max_f32_e64 v173, |v182|, |v183|
	v_add_f32_e32 v155, v155, v159
	v_max3_f32 v159, |v170|, |v171|, v166
	v_add_f32_e32 v166, v186, v187
	v_max3_f32 v167, |v174|, |v175|, v167
	v_fmac_f32_e32 v190, v82, v82
	v_fmac_f32_e32 v191, v84, v84
	v_add_f32_e32 v170, v188, v189
	v_max3_f32 v171, |v180|, |v181|, v172
	v_max3_f32 v173, |v184|, |v185|, v173
	v_add_f32_e32 v155, v155, v166
	v_max3_f32 v159, v159, 0, v167
	v_add_f32_e32 v172, v190, v191
	v_add_f32_e32 v155, v155, v170
	v_max3_f32 v166, v159, v171, v173
	v_add_f32_e32 v155, v155, v172
	ds_bpermute_b32 v167, v169, v166
	ds_bpermute_b32 v171, v169, v155
	v_cvt_pk_bf16_f32 v156, v94, v95
	v_cvt_pk_bf16_f32 v157, v96, v97
	v_cvt_pk_bf16_f32 v158, v90, v91
	v_cvt_pk_bf16_f32 v159, v92, v93
	global_store_dwordx4 v[160:161], v[156:159], off
	v_cvt_pk_bf16_f32 v170, v86, v87
	v_cvt_pk_bf16_f32 v172, v82, v83
	s_waitcnt lgkmcnt(1)
	v_max_f32_e32 v157, v167, v167
	s_waitcnt lgkmcnt(0)
	v_add_f32_e32 v156, v155, v171
	v_max_f32_e32 v155, v166, v157
	ds_bpermute_b32 v157, v168, v156
	ds_bpermute_b32 v158, v168, v155
	v_cvt_pk_bf16_f32 v171, v88, v89
	v_cvt_pk_bf16_f32 v173, v84, v85
	global_store_dwordx4 v[160:161], v[170:173], off offset:256
	s_and_saveexec_b64 s[14:15], s[2:3]
	s_cbranch_execz .LBB0_991
	v_lshl_add_u32 v159, v154, 5, s11
	s_waitcnt lgkmcnt(1)
	v_add_f32_e32 v154, v156, v157
	s_waitcnt lgkmcnt(0)
	v_max_f32_e32 v156, v158, v158
	v_max_f32_e32 v155, v155, v155
	v_max_f32_e32 v155, v155, v156
	ds_write_b64 v159, v[154:155]
.LBB0_991:
	s_or_b64 exec, exec, s[14:15]
	v_add_u32_e32 v156, 0x90, v177
	v_add_u32_e32 v154, s10, v156
	v_mov_b32_e32 v155, v153
	s_waitcnt lgkmcnt(0)
	v_lshlrev_b64 v[158:159], 12, v[154:155]
	v_lshl_add_u64 v[158:159], s[22:23], 0, v[158:159]
	v_lshl_add_u64 v[166:167], v[162:163], 1, v[158:159]
	s_mov_b32 s98, 0xb0000
	s_mov_b32 s99, 0
	v_lshl_add_u64 v[230:231], v[248:249], 0, s[98:99]
	global_load_dwordx4 v[226:229], v[230:231], off
	global_load_dwordx4 v[230:233], v[230:231], off offset:256
	s_waitcnt vmcnt(9)
	v_mov_b32_e32 v158, v234
	v_mov_b32_e32 v159, v235
	v_mov_b32_e32 v160, v236
	v_mov_b32_e32 v161, v237
	v_lshlrev_b32_e32 v174, 16, v158
	v_and_b32_e32 v175, 0xffff0000, v158
	v_lshlrev_b32_e32 v158, 16, v159
	v_and_b32_e32 v159, 0xffff0000, v159
	v_lshlrev_b32_e32 v178, 16, v160
	v_and_b32_e32 v179, 0xffff0000, v160
	v_lshlrev_b32_e32 v160, 16, v161
	v_and_b32_e32 v161, 0xffff0000, v161
	s_waitcnt vmcnt(8)
	v_mov_b32_e32 v170, v238
	v_mov_b32_e32 v171, v239
	v_mov_b32_e32 v172, v240
	v_mov_b32_e32 v173, v241
	v_lshlrev_b32_e32 v180, 16, v170
	v_and_b32_e32 v181, 0xffff0000, v170
	v_lshlrev_b32_e32 v170, 16, v171
	v_and_b32_e32 v171, 0xffff0000, v171
	v_lshlrev_b32_e32 v182, 16, v172
	v_and_b32_e32 v183, 0xffff0000, v172
	v_lshlrev_b32_e32 v172, 16, v173
	v_and_b32_e32 v173, 0xffff0000, v173
	v_pk_fma_f32 v[80:81], v[80:81], s[0:1], v[158:159] op_sel_hi:[1,0,1]
	v_pk_fma_f32 v[78:79], v[78:79], s[0:1], v[174:175] op_sel_hi:[1,0,1]
	v_pk_fma_f32 v[76:77], v[76:77], s[0:1], v[160:161] op_sel_hi:[1,0,1]
	v_pk_fma_f32 v[74:75], v[74:75], s[0:1], v[178:179] op_sel_hi:[1,0,1]
	v_pk_fma_f32 v[72:73], v[72:73], s[0:1], v[170:171] op_sel_hi:[1,0,1]
	v_pk_fma_f32 v[70:71], v[70:71], s[0:1], v[180:181] op_sel_hi:[1,0,1]
	v_pk_fma_f32 v[68:69], v[68:69], s[0:1], v[172:173] op_sel_hi:[1,0,1]
	v_mul_f32_e32 v157, v79, v79
	v_mul_f32_e32 v161, v81, v81
	v_pk_mul_f32 v[170:171], v[16:17], v[80:81]
	v_mul_f32_e32 v188, v75, v75
	v_mul_f32_e32 v189, v77, v77
	v_pk_mul_f32 v[174:175], v[12:13], v[76:77]
	v_pk_fma_f32 v[66:67], v[66:67], s[0:1], v[182:183] op_sel_hi:[1,0,1]
	v_pk_mul_f32 v[172:173], v[14:15], v[78:79]
	v_pk_mul_f32 v[178:179], v[10:11], v[74:75]
	v_mul_f32_e32 v190, v71, v71
	v_mul_f32_e32 v191, v73, v73
	v_pk_mul_f32 v[180:181], v[8:9], v[72:73]
	v_pk_mul_f32 v[184:185], v[4:5], v[68:69]
	v_fmac_f32_e32 v157, v78, v78
	v_fmac_f32_e32 v161, v80, v80
	v_max_f32_e64 v170, |v170|, |v171|
	v_fmac_f32_e32 v188, v74, v74
	v_fmac_f32_e32 v189, v76, v76
	v_max_f32_e64 v171, |v174|, |v175|
	v_pk_mul_f32 v[182:183], v[6:7], v[70:71]
	v_mul_f32_e32 v192, v67, v67
	v_mul_f32_e32 v193, v69, v69
	v_pk_mul_f32 v[186:187], v[2:3], v[66:67]
	v_fmac_f32_e32 v190, v70, v70
	v_fmac_f32_e32 v191, v72, v72
	v_max_f32_e64 v174, |v180|, |v181|
	v_max_f32_e64 v175, |v184|, |v185|
	v_add_f32_e32 v157, v157, v161
	v_max3_f32 v161, |v172|, |v173|, v170
	v_add_f32_e32 v170, v188, v189
	v_max3_f32 v171, |v178|, |v179|, v171
	v_fmac_f32_e32 v192, v66, v66
	v_fmac_f32_e32 v193, v68, v68
	v_add_f32_e32 v172, v190, v191
	v_max3_f32 v173, |v182|, |v183|, v174
	v_max3_f32 v175, |v186|, |v187|, v175
	v_add_f32_e32 v157, v157, v170
	v_max3_f32 v161, v161, 0, v171
	v_add_f32_e32 v174, v192, v193
	v_add_f32_e32 v157, v157, v172
	v_max3_f32 v171, v161, v173, v175
	v_add_f32_e32 v157, v157, v174
	ds_bpermute_b32 v172, v169, v171
	ds_bpermute_b32 v173, v169, v157
	v_cvt_pk_bf16_f32 v158, v78, v79
	v_cvt_pk_bf16_f32 v159, v80, v81
	v_cvt_pk_bf16_f32 v160, v74, v75
	v_cvt_pk_bf16_f32 v161, v76, v77
	global_store_dwordx4 v[166:167], v[158:161], off
	v_cvt_pk_bf16_f32 v170, v70, v71
	s_waitcnt lgkmcnt(1)
	v_max_f32_e32 v159, v172, v172
	s_waitcnt lgkmcnt(0)
	v_add_f32_e32 v158, v157, v173
	v_max_f32_e32 v157, v171, v159
	ds_bpermute_b32 v159, v168, v158
	ds_bpermute_b32 v160, v168, v157
	v_cvt_pk_bf16_f32 v171, v72, v73
	v_cvt_pk_bf16_f32 v172, v66, v67
	v_cvt_pk_bf16_f32 v173, v68, v69
	global_store_dwordx4 v[166:167], v[170:173], off offset:256
	s_and_saveexec_b64 s[0:1], s[2:3]
	s_cbranch_execz .LBB0_993
	v_lshl_add_u32 v161, v156, 5, s11
	s_waitcnt lgkmcnt(1)
	v_add_f32_e32 v156, v158, v159
	s_waitcnt lgkmcnt(0)
	v_max_f32_e32 v158, v160, v160
	v_max_f32_e32 v157, v157, v157
	v_max_f32_e32 v157, v157, v158
	ds_write_b64 v161, v[156:157]
.LBB0_993:
	s_or_b64 exec, exec, s[0:1]
	v_add_u32_e32 v158, 0xa0, v177
	v_add_u32_e32 v156, s10, v158
	v_mov_b32_e32 v157, 0
	s_waitcnt lgkmcnt(0)
	v_lshlrev_b64 v[160:161], 12, v[156:157]
	v_lshl_add_u64 v[160:161], s[22:23], 0, v[160:161]
	v_lshl_add_u64 v[174:175], v[162:163], 1, v[160:161]
	s_brev_b32 s0, 60
	s_waitcnt vmcnt(7)
	v_mov_b32_e32 v170, v218
	v_mov_b32_e32 v171, v219
	v_mov_b32_e32 v172, v220
	v_mov_b32_e32 v173, v221
	v_lshlrev_b32_e32 v160, 16, v170
	v_and_b32_e32 v161, 0xffff0000, v170
	v_lshlrev_b32_e32 v166, 16, v171
	v_and_b32_e32 v167, 0xffff0000, v171
	v_lshlrev_b32_e32 v170, 16, v172
	v_and_b32_e32 v171, 0xffff0000, v172
	v_lshlrev_b32_e32 v172, 16, v173
	v_and_b32_e32 v173, 0xffff0000, v173
	s_waitcnt vmcnt(6)
	v_mov_b32_e32 v178, v222
	v_mov_b32_e32 v179, v223
	v_mov_b32_e32 v180, v224
	v_mov_b32_e32 v181, v225
	v_lshlrev_b32_e32 v182, 16, v178
	v_and_b32_e32 v183, 0xffff0000, v178
	v_lshlrev_b32_e32 v178, 16, v179
	v_and_b32_e32 v179, 0xffff0000, v179
	v_lshlrev_b32_e32 v184, 16, v180
	v_and_b32_e32 v185, 0xffff0000, v180
	v_lshlrev_b32_e32 v180, 16, v181
	v_and_b32_e32 v181, 0xffff0000, v181
	v_pk_fma_f32 v[64:65], v[64:65], s[0:1], v[166:167] op_sel_hi:[1,0,1]
	v_pk_fma_f32 v[62:63], v[62:63], s[0:1], v[160:161] op_sel_hi:[1,0,1]
	v_pk_fma_f32 v[60:61], v[60:61], s[0:1], v[172:173] op_sel_hi:[1,0,1]
	v_pk_fma_f32 v[58:59], v[58:59], s[0:1], v[170:171] op_sel_hi:[1,0,1]
	v_pk_fma_f32 v[56:57], v[56:57], s[0:1], v[178:179] op_sel_hi:[1,0,1]
	v_pk_fma_f32 v[54:55], v[54:55], s[0:1], v[182:183] op_sel_hi:[1,0,1]
	v_pk_fma_f32 v[52:53], v[52:53], s[0:1], v[180:181] op_sel_hi:[1,0,1]
	v_mul_f32_e32 v159, v63, v63
	v_mul_f32_e32 v173, v65, v65
	v_pk_mul_f32 v[160:161], v[16:17], v[64:65]
	v_mul_f32_e32 v190, v59, v59
	v_mul_f32_e32 v191, v61, v61
	v_pk_mul_f32 v[178:179], v[12:13], v[60:61]
	v_pk_fma_f32 v[50:51], v[50:51], s[0:1], v[184:185] op_sel_hi:[1,0,1]
	v_pk_mul_f32 v[166:167], v[14:15], v[62:63]
	v_pk_mul_f32 v[180:181], v[10:11], v[58:59]
	v_mul_f32_e32 v192, v55, v55
	v_mul_f32_e32 v193, v57, v57
	v_pk_mul_f32 v[182:183], v[8:9], v[56:57]
	v_pk_mul_f32 v[186:187], v[4:5], v[52:53]
	v_fmac_f32_e32 v159, v62, v62
	v_fmac_f32_e32 v173, v64, v64
	v_max_f32_e64 v160, |v160|, |v161|
	v_fmac_f32_e32 v190, v58, v58
	v_fmac_f32_e32 v191, v60, v60
	v_max_f32_e64 v161, |v178|, |v179|
	v_pk_mul_f32 v[184:185], v[6:7], v[54:55]
	v_mul_f32_e32 v194, v51, v51
	v_mul_f32_e32 v195, v53, v53
	v_pk_mul_f32 v[188:189], v[2:3], v[50:51]
	v_fmac_f32_e32 v192, v54, v54
	v_fmac_f32_e32 v193, v56, v56
	v_max_f32_e64 v178, |v182|, |v183|
	v_max_f32_e64 v179, |v186|, |v187|
	v_add_f32_e32 v159, v159, v173
	v_max3_f32 v160, |v166|, |v167|, v160
	v_add_f32_e32 v166, v190, v191
	v_max3_f32 v161, |v180|, |v181|, v161
	v_fmac_f32_e32 v194, v50, v50
	v_fmac_f32_e32 v195, v52, v52
	v_add_f32_e32 v167, v192, v193
	v_max3_f32 v173, |v184|, |v185|, v178
	v_max3_f32 v179, |v188|, |v189|, v179
	v_add_f32_e32 v159, v159, v166
	v_max3_f32 v160, v160, 0, v161
	v_add_f32_e32 v178, v194, v195
	v_add_f32_e32 v159, v159, v167
	v_max3_f32 v161, v160, v173, v179
	v_add_f32_e32 v159, v159, v178
	ds_bpermute_b32 v160, v169, v161
	ds_bpermute_b32 v166, v169, v159
	v_cvt_pk_bf16_f32 v170, v62, v63
	v_cvt_pk_bf16_f32 v171, v64, v65
	v_cvt_pk_bf16_f32 v172, v58, v59
	s_waitcnt lgkmcnt(1)
	v_max_f32_e32 v167, v160, v160
	s_waitcnt lgkmcnt(0)
	v_add_f32_e32 v160, v159, v166
	v_max_f32_e32 v159, v161, v167
	ds_bpermute_b32 v161, v168, v160
	ds_bpermute_b32 v166, v168, v159
	v_cvt_pk_bf16_f32 v173, v60, v61
	v_cvt_pk_bf16_f32 v178, v54, v55
	v_cvt_pk_bf16_f32 v179, v56, v57
	v_cvt_pk_bf16_f32 v180, v50, v51
	v_cvt_pk_bf16_f32 v181, v52, v53
	global_store_dwordx4 v[174:175], v[170:173], off
	global_store_dwordx4 v[174:175], v[178:181], off offset:256
	s_and_saveexec_b64 s[14:15], s[2:3]
	s_cbranch_execz .LBB0_995
	v_lshl_add_u32 v167, v158, 5, s11
	s_waitcnt lgkmcnt(1)
	v_add_f32_e32 v158, v160, v161
	s_waitcnt lgkmcnt(0)
	v_max_f32_e32 v160, v166, v166
	v_max_f32_e32 v159, v159, v159
	v_max_f32_e32 v159, v159, v160
	ds_write_b64 v167, v[158:159]
.LBB0_995:
	s_or_b64 exec, exec, s[14:15]
	v_add_u32_e32 v160, 0xb0, v177
	v_add_u32_e32 v158, s10, v160
	v_mov_b32_e32 v159, v157
	s_waitcnt lgkmcnt(0)
	v_lshlrev_b64 v[166:167], 12, v[158:159]
	v_lshl_add_u64 v[166:167], s[22:23], 0, v[166:167]
	v_lshl_add_u64 v[174:175], v[162:163], 1, v[166:167]
	s_waitcnt vmcnt(5)
	v_mov_b32_e32 v170, v226
	v_mov_b32_e32 v171, v227
	v_mov_b32_e32 v172, v228
	v_mov_b32_e32 v173, v229
	v_lshlrev_b32_e32 v166, 16, v170
	v_and_b32_e32 v167, 0xffff0000, v170
	v_lshlrev_b32_e32 v170, 16, v171
	v_and_b32_e32 v171, 0xffff0000, v171
	v_lshlrev_b32_e32 v182, 16, v172
	v_and_b32_e32 v183, 0xffff0000, v172
	v_lshlrev_b32_e32 v172, 16, v173
	v_and_b32_e32 v173, 0xffff0000, v173
	s_waitcnt vmcnt(4)
	v_mov_b32_e32 v178, v230
	v_mov_b32_e32 v179, v231
	v_mov_b32_e32 v180, v232
	v_mov_b32_e32 v181, v233
	v_lshlrev_b32_e32 v184, 16, v178
	v_and_b32_e32 v185, 0xffff0000, v178
	v_lshlrev_b32_e32 v178, 16, v179
	v_and_b32_e32 v179, 0xffff0000, v179
	v_lshlrev_b32_e32 v186, 16, v180
	v_and_b32_e32 v187, 0xffff0000, v180
	v_lshlrev_b32_e32 v180, 16, v181
	v_and_b32_e32 v181, 0xffff0000, v181
	v_pk_fma_f32 v[48:49], v[48:49], s[0:1], v[170:171] op_sel_hi:[1,0,1]
	v_pk_fma_f32 v[46:47], v[46:47], s[0:1], v[166:167] op_sel_hi:[1,0,1]
	v_pk_fma_f32 v[44:45], v[44:45], s[0:1], v[172:173] op_sel_hi:[1,0,1]
	v_pk_fma_f32 v[42:43], v[42:43], s[0:1], v[182:183] op_sel_hi:[1,0,1]
	v_pk_fma_f32 v[40:41], v[40:41], s[0:1], v[178:179] op_sel_hi:[1,0,1]
	v_pk_fma_f32 v[38:39], v[38:39], s[0:1], v[184:185] op_sel_hi:[1,0,1]
	v_pk_fma_f32 v[36:37], v[36:37], s[0:1], v[180:181] op_sel_hi:[1,0,1]
	v_mul_f32_e32 v161, v47, v47
	v_mul_f32_e32 v173, v49, v49
	v_pk_mul_f32 v[166:167], v[16:17], v[48:49]
	v_mul_f32_e32 v192, v43, v43
	v_mul_f32_e32 v193, v45, v45
	v_pk_mul_f32 v[180:181], v[12:13], v[44:45]
	v_pk_fma_f32 v[34:35], v[34:35], s[0:1], v[186:187] op_sel_hi:[1,0,1]
	v_pk_mul_f32 v[178:179], v[14:15], v[46:47]
	v_pk_mul_f32 v[182:183], v[10:11], v[42:43]
	v_mul_f32_e32 v194, v39, v39
	v_mul_f32_e32 v195, v41, v41
	v_pk_mul_f32 v[184:185], v[8:9], v[40:41]
	v_pk_mul_f32 v[188:189], v[4:5], v[36:37]
	v_fmac_f32_e32 v161, v46, v46
	v_fmac_f32_e32 v173, v48, v48
	v_max_f32_e64 v166, |v166|, |v167|
	v_fmac_f32_e32 v192, v42, v42
	v_fmac_f32_e32 v193, v44, v44
	v_max_f32_e64 v167, |v180|, |v181|
	v_pk_mul_f32 v[186:187], v[6:7], v[38:39]
	v_mul_f32_e32 v196, v35, v35
	v_mul_f32_e32 v197, v37, v37
	v_pk_mul_f32 v[190:191], v[2:3], v[34:35]
	v_fmac_f32_e32 v194, v38, v38
	v_fmac_f32_e32 v195, v40, v40
	v_max_f32_e64 v180, |v184|, |v185|
	v_max_f32_e64 v181, |v188|, |v189|
	v_add_f32_e32 v161, v161, v173
	v_max3_f32 v166, |v178|, |v179|, v166
	v_add_f32_e32 v173, v192, v193
	v_max3_f32 v167, |v182|, |v183|, v167
	v_fmac_f32_e32 v196, v34, v34
	v_fmac_f32_e32 v197, v36, v36
	v_add_f32_e32 v178, v194, v195
	v_max3_f32 v179, |v186|, |v187|, v180
	v_max3_f32 v181, |v190|, |v191|, v181
	v_add_f32_e32 v161, v161, v173
	v_max3_f32 v166, v166, 0, v167
	v_add_f32_e32 v180, v196, v197
	v_add_f32_e32 v161, v161, v178
	v_max3_f32 v167, v166, v179, v181
	v_add_f32_e32 v161, v161, v180
	ds_bpermute_b32 v166, v169, v167
	ds_bpermute_b32 v169, v169, v161
	v_cvt_pk_bf16_f32 v170, v46, v47
	v_cvt_pk_bf16_f32 v171, v48, v49
	v_cvt_pk_bf16_f32 v172, v42, v43
	v_cvt_pk_bf16_f32 v173, v44, v45
	global_store_dwordx4 v[174:175], v[170:173], off
	v_cvt_pk_bf16_f32 v178, v38, v39
	v_cvt_pk_bf16_f32 v179, v40, v41
	s_waitcnt lgkmcnt(1)
	v_max_f32_e32 v170, v166, v166
	s_waitcnt lgkmcnt(0)
	v_add_f32_e32 v166, v161, v169
	v_max_f32_e32 v161, v167, v170
	ds_bpermute_b32 v167, v168, v166
	ds_bpermute_b32 v168, v168, v161
	v_cvt_pk_bf16_f32 v180, v34, v35
	v_cvt_pk_bf16_f32 v181, v36, v37
	global_store_dwordx4 v[174:175], v[178:181], off offset:256
	s_and_saveexec_b64 s[0:1], s[2:3]
	s_cbranch_execz .LBB0_997
	v_lshl_add_u32 v169, v160, 5, s11
	s_waitcnt lgkmcnt(1)
	v_add_f32_e32 v160, v166, v167
	s_waitcnt lgkmcnt(0)
	v_max_f32_e32 v166, v168, v168
	v_max_f32_e32 v161, v161, v161
	v_max_f32_e32 v161, v161, v166
	ds_write_b64 v169, v[160:161]

.LBB0_1459:
	v_readlane_b32 s0, v251, 28
	s_lshl_b32 s2, s0, 3
	s_add_i32 s0, s2, s10
	v_lshlrev_b32_e32 v2, 4, v1
	s_ashr_i32 s1, s0, 31
	v_lshl_add_u64 v[4:5], s[24:25], 0, v[2:3]
	s_lshl_b64 s[4:5], s[0:1], 11
	s_waitcnt vmcnt(11)
	v_lshl_add_u64 v[18:19], v[4:5], 0, s[4:5]
	s_waitcnt lgkmcnt(0)
	s_barrier
	s_mov_b32 s98, 0x1000
	s_mov_b32 s99, 0
	v_lshl_add_u64 v[128:129], v[18:19], 0, s[98:99]
	s_mov_b32 s98, 0x2000
	s_mov_b32 s99, 0
	v_lshl_add_u64 v[130:131], v[18:19], 0, s[98:99]
	s_mov_b32 s98, 0x3000
	s_mov_b32 s99, 0
	v_lshl_add_u64 v[132:133], v[18:19], 0, s[98:99]
	global_load_dwordx4 v[64:67], v[18:19], off
	global_load_dwordx4 v[68:71], v[18:19], off offset:1024
	global_load_dwordx4 v[72:75], v[18:19], off offset:2048
	global_load_dwordx4 v[76:79], v[18:19], off offset:3072
	global_load_dwordx4 v[80:83], v[128:129], off
	global_load_dwordx4 v[84:87], v[128:129], off offset:1024
	global_load_dwordx4 v[88:91], v[128:129], off offset:2048
	global_load_dwordx4 v[92:95], v[128:129], off offset:3072
	global_load_dwordx4 v[96:99], v[130:131], off
	global_load_dwordx4 v[100:103], v[130:131], off offset:1024
	global_load_dwordx4 v[104:107], v[130:131], off offset:2048
	global_load_dwordx4 v[108:111], v[130:131], off offset:3072
	global_load_dwordx4 v[112:115], v[132:133], off
	global_load_dwordx4 v[116:119], v[132:133], off offset:1024
	global_load_dwordx4 v[120:123], v[132:133], off offset:2048
	global_load_dwordx4 v[124:127], v[132:133], off offset:3072
	v_readlane_b32 s1, v251, 27
	s_andn2_b32 s1, s1, 63
	s_add_i32 s1, s1, 0
	v_mov_b32_e32 v10, s1
	ds_read_b128 v[10:13], v10 offset:8320
	s_or_b32 s3, s2, 2
	s_lshl_b32 s1, s3, 3
	s_add_i32 s1, s1, 0
	v_mov_b32_e32 v14, s1
	ds_read_b128 v[14:17], v14 offset:8320
	s_waitcnt lgkmcnt(1)
	v_ashrrev_i32_e32 v21, 31, v10
	v_mov_b32_e32 v20, v10
	v_lshl_add_u64 v[2:3], s[26:27], 0, v[2:3]
	s_waitcnt vmcnt(11)
	v_ashrrev_i32_e32 v23, 31, v11
	v_mov_b32_e32 v22, v11
	v_lshlrev_b64 v[20:21], 11, v[20:21]
	v_lshlrev_b64 v[10:11], 11, v[22:23]
	v_lshl_add_u64 v[20:21], v[2:3], 0, v[20:21]
	v_lshl_add_u64 v[10:11], v[2:3], 0, v[10:11]
	s_add_i32 s4, s0, 1
	s_ashr_i32 s5, s4, 31
	s_lshl_b64 s[4:5], s[4:5], 11
	s_or_b32 s1, s2, 4
	s_waitcnt vmcnt(15)
	global_store_dwordx4 v[20:21], v[64:67], off
	global_store_dwordx4 v[10:11], v[64:67], off
	v_lshl_add_u64 v[18:19], v[4:5], 0, s[4:5]
	s_add_i32 s4, s3, s10
	s_ashr_i32 s5, s4, 31
	s_lshl_b64 s[4:5], s[4:5], 11
	s_waitcnt vmcnt(16)
	global_store_dwordx4 v[20:21], v[68:71], off offset:1024
	global_store_dwordx4 v[10:11], v[68:71], off offset:1024
	v_ashrrev_i32_e32 v11, 31, v12
	v_mov_b32_e32 v10, v12
	v_ashrrev_i32_e32 v21, 31, v13
	v_mov_b32_e32 v20, v13
	v_lshlrev_b64 v[10:11], 11, v[10:11]
	v_lshlrev_b64 v[12:13], 11, v[20:21]
	v_lshl_add_u64 v[10:11], v[2:3], 0, v[10:11]
	v_lshl_add_u64 v[12:13], v[2:3], 0, v[12:13]
	s_waitcnt vmcnt(17)
	global_store_dwordx4 v[10:11], v[72:75], off
	global_store_dwordx4 v[12:13], v[72:75], off
	v_lshl_add_u64 v[18:19], v[4:5], 0, s[4:5]
	s_add_i32 s4, s0, 3
	s_ashr_i32 s5, s4, 31
	s_lshl_b64 s[4:5], s[4:5], 11
	s_waitcnt vmcnt(18)
	global_store_dwordx4 v[10:11], v[76:79], off offset:1024
	global_store_dwordx4 v[12:13], v[76:79], off offset:1024
	s_waitcnt lgkmcnt(0)
	v_ashrrev_i32_e32 v11, 31, v14
	v_mov_b32_e32 v10, v14
	v_ashrrev_i32_e32 v13, 31, v15
	v_mov_b32_e32 v12, v15
	v_lshlrev_b64 v[10:11], 11, v[10:11]
	v_lshlrev_b64 v[12:13], 11, v[12:13]
	v_lshl_add_u64 v[10:11], v[2:3], 0, v[10:11]
	v_lshl_add_u64 v[12:13], v[2:3], 0, v[12:13]
	v_lshl_add_u64 v[14:15], v[4:5], 0, s[4:5]
	s_add_i32 s4, s1, s10
	s_ashr_i32 s5, s4, 31
	s_lshl_b64 s[4:5], s[4:5], 11
	s_lshl_b32 s1, s1, 3
	s_add_i32 s1, s1, 0
	s_waitcnt vmcnt(19)
	global_store_dwordx4 v[10:11], v[80:83], off
	global_store_dwordx4 v[12:13], v[80:83], off
	v_lshl_add_u64 v[18:19], v[4:5], 0, s[4:5]
	s_or_b32 s4, s2, 6
	s_add_i32 s2, s0, 5
	s_ashr_i32 s3, s2, 31
	s_lshl_b64 s[2:3], s[2:3], 11
	s_add_i32 s0, s0, 7
	s_waitcnt vmcnt(20)
	global_store_dwordx4 v[10:11], v[84:87], off offset:1024
	global_store_dwordx4 v[12:13], v[84:87], off offset:1024
	v_ashrrev_i32_e32 v11, 31, v16
	v_mov_b32_e32 v10, v16
	v_ashrrev_i32_e32 v13, 31, v17
	v_mov_b32_e32 v12, v17
	v_lshlrev_b64 v[10:11], 11, v[10:11]
	v_lshlrev_b64 v[12:13], 11, v[12:13]
	v_lshl_add_u64 v[10:11], v[2:3], 0, v[10:11]
	v_lshl_add_u64 v[12:13], v[2:3], 0, v[12:13]
	s_waitcnt vmcnt(21)
	global_store_dwordx4 v[10:11], v[88:91], off
	global_store_dwordx4 v[12:13], v[88:91], off
	s_waitcnt vmcnt(22)
	global_store_dwordx4 v[10:11], v[92:95], off offset:1024
	global_store_dwordx4 v[12:13], v[92:95], off offset:1024
	v_mov_b32_e32 v10, s1
	ds_read_b128 v[10:13], v10 offset:8320
	s_lshl_b32 s1, s4, 3
	s_add_i32 s1, s1, 0
	v_mov_b32_e32 v14, s1
	ds_read_b128 v[14:17], v14 offset:8320
	s_waitcnt lgkmcnt(1)
	v_ashrrev_i32_e32 v21, 31, v10
	v_mov_b32_e32 v20, v10
	v_ashrrev_i32_e32 v23, 31, v11
	v_mov_b32_e32 v22, v11
	v_lshlrev_b64 v[20:21], 11, v[20:21]
	v_lshlrev_b64 v[10:11], 11, v[22:23]
	v_lshl_add_u64 v[20:21], v[2:3], 0, v[20:21]
	v_lshl_add_u64 v[10:11], v[2:3], 0, v[10:11]
	s_ashr_i32 s1, s0, 31
	s_lshl_b64 s[0:1], s[0:1], 11
	s_waitcnt vmcnt(23)
	global_store_dwordx4 v[20:21], v[96:99], off
	global_store_dwordx4 v[10:11], v[96:99], off
	v_lshl_add_u64 v[18:19], v[4:5], 0, s[2:3]
	s_add_i32 s2, s4, s10
	s_ashr_i32 s3, s2, 31
	s_lshl_b64 s[2:3], s[2:3], 11
	s_waitcnt vmcnt(24)
	global_store_dwordx4 v[20:21], v[100:103], off offset:1024
	global_store_dwordx4 v[10:11], v[100:103], off offset:1024
	v_ashrrev_i32_e32 v11, 31, v12
	v_mov_b32_e32 v10, v12
	v_ashrrev_i32_e32 v21, 31, v13
	v_mov_b32_e32 v20, v13
	v_lshlrev_b64 v[10:11], 11, v[10:11]
	v_lshlrev_b64 v[12:13], 11, v[20:21]
	v_lshl_add_u64 v[10:11], v[2:3], 0, v[10:11]
	v_lshl_add_u64 v[12:13], v[2:3], 0, v[12:13]
	s_waitcnt vmcnt(25)
	global_store_dwordx4 v[10:11], v[104:107], off
	global_store_dwordx4 v[12:13], v[104:107], off
	v_lshl_add_u64 v[18:19], v[4:5], 0, s[2:3]
	s_waitcnt vmcnt(26)
	global_store_dwordx4 v[10:11], v[108:111], off offset:1024
	global_store_dwordx4 v[12:13], v[108:111], off offset:1024
	s_waitcnt lgkmcnt(0)
	v_ashrrev_i32_e32 v11, 31, v14
	v_mov_b32_e32 v10, v14
	v_ashrrev_i32_e32 v13, 31, v15
	v_mov_b32_e32 v12, v15
	v_lshlrev_b64 v[10:11], 11, v[10:11]
	v_lshlrev_b64 v[12:13], 11, v[12:13]
	v_lshl_add_u64 v[10:11], v[2:3], 0, v[10:11]
	v_lshl_add_u64 v[12:13], v[2:3], 0, v[12:13]
	v_lshl_add_u64 v[14:15], v[4:5], 0, s[0:1]
	s_waitcnt vmcnt(27)
	global_store_dwordx4 v[10:11], v[112:115], off
	global_store_dwordx4 v[12:13], v[112:115], off
	s_waitcnt vmcnt(28)
	global_store_dwordx4 v[10:11], v[116:119], off offset:1024
	global_store_dwordx4 v[12:13], v[116:119], off offset:1024
	s_nop 0
	v_ashrrev_i32_e32 v9, 31, v16
	v_mov_b32_e32 v8, v16
	v_ashrrev_i32_e32 v11, 31, v17
	v_mov_b32_e32 v10, v17
	v_lshlrev_b64 v[8:9], 11, v[8:9]
	v_lshlrev_b64 v[10:11], 11, v[10:11]
	v_lshl_add_u64 v[8:9], v[2:3], 0, v[8:9]
	v_lshl_add_u64 v[10:11], v[2:3], 0, v[10:11]
	s_waitcnt vmcnt(29)
	global_store_dwordx4 v[8:9], v[120:123], off
	global_store_dwordx4 v[10:11], v[120:123], off
	s_waitcnt vmcnt(30)
	global_store_dwordx4 v[8:9], v[124:127], off offset:1024
	global_store_dwordx4 v[10:11], v[124:127], off offset:1024
